# GEMM main loops: the per-cluster s_setprio 1 / s_setprio 0 flips around the MFMA clusters removed
# baseline (speedup 1.0000x reference)
.LBB0_242:
	ds_read_b128 v[132:135], v206
	ds_read_b128 v[136:139], v206 offset:1024
	ds_read_b128 v[140:143], v206 offset:2048
	ds_read_b128 v[144:147], v206 offset:3072
	ds_read_b128 v[148:151], v206 offset:16384
	ds_read_b128 v[152:155], v206 offset:17408
	ds_read_b128 v[156:159], v206 offset:18432
	ds_read_b128 v[160:163], v206 offset:19456
	s_add_i32 s3, s0, 0xfffc0080
	s_cmp_eq_u32 s2, 12
	s_cselect_b32 s9, s79, s3
	s_cselect_b32 s8, s85, s1
	s_add_i32 s3, s9, 0x80
	s_mov_b32 s56, s50
	s_mov_b32 m0, s54
	ds_read_b128 v[174:177], v207
	ds_read_b128 v[178:181], v207 offset:1024
	ds_read_b128 v[208:211], v207 offset:2048
	ds_read_b128 v[212:215], v207 offset:3072
	ds_read_b128 v[216:219], v207 offset:4096
	ds_read_b128 v[224:227], v207 offset:5120
	ds_read_b128 v[228:231], v207 offset:6144
	ds_read_b128 v[232:235], v207 offset:7168
	buffer_load_dwordx4 v166, s[56:59], s0 offen lds
	s_mov_b32 m0, s76
	s_nop 0
	buffer_load_dwordx4 v182, s[56:59], s0 offen lds
	s_waitcnt vmcnt(8)
	s_waitcnt lgkmcnt(0)
	s_barrier
	s_waitcnt lgkmcnt(7)
	v_mfma_i32_16x16x64_i8 v[124:127], v[132:135], v[174:177], v[124:127]
	v_mfma_i32_16x16x64_i8 v[120:123], v[140:143], v[174:177], v[120:123]
	s_waitcnt lgkmcnt(5)
	v_mfma_i32_16x16x64_i8 v[116:119], v[132:135], v[208:211], v[116:119]
	v_mfma_i32_16x16x64_i8 v[112:115], v[140:143], v[208:211], v[112:115]
	s_waitcnt lgkmcnt(3)
	v_mfma_i32_16x16x64_i8 v[108:111], v[132:135], v[216:219], v[108:111]
	v_mfma_i32_16x16x64_i8 v[104:107], v[140:143], v[216:219], v[104:107]
	s_waitcnt lgkmcnt(1)
	v_mfma_i32_16x16x64_i8 v[100:103], v[132:135], v[228:231], v[100:103]
	v_mfma_i32_16x16x64_i8 v[96:99], v[140:143], v[228:231], v[96:99]
	v_mfma_i32_16x16x64_i8 v[124:127], v[136:139], v[178:181], v[124:127]
	v_mfma_i32_16x16x64_i8 v[120:123], v[144:147], v[178:181], v[120:123]
	v_mfma_i32_16x16x64_i8 v[116:119], v[136:139], v[212:215], v[116:119]
	v_mfma_i32_16x16x64_i8 v[112:115], v[144:147], v[212:215], v[112:115]
	v_mfma_i32_16x16x64_i8 v[108:111], v[136:139], v[224:227], v[108:111]
	v_mfma_i32_16x16x64_i8 v[104:107], v[144:147], v[224:227], v[104:107]
	s_waitcnt lgkmcnt(0)
	v_mfma_i32_16x16x64_i8 v[100:103], v[136:139], v[232:235], v[100:103]
	v_mfma_i32_16x16x64_i8 v[96:99], v[144:147], v[232:235], v[96:99]
	v_mfma_i32_16x16x64_i8 v[92:95], v[148:151], v[174:177], v[92:95]
	v_mfma_i32_16x16x64_i8 v[88:91], v[156:159], v[174:177], v[88:91]
	v_mfma_i32_16x16x64_i8 v[84:87], v[148:151], v[208:211], v[84:87]
	v_mfma_i32_16x16x64_i8 v[80:83], v[156:159], v[208:211], v[80:83]
	v_mfma_i32_16x16x64_i8 v[76:79], v[148:151], v[216:219], v[76:79]
	v_mfma_i32_16x16x64_i8 v[72:75], v[156:159], v[216:219], v[72:75]
	v_mfma_i32_16x16x64_i8 v[68:71], v[148:151], v[228:231], v[68:71]
	v_mfma_i32_16x16x64_i8 v[64:67], v[156:159], v[228:231], v[64:67]
	v_mfma_i32_16x16x64_i8 v[92:95], v[152:155], v[178:181], v[92:95]
	v_mfma_i32_16x16x64_i8 v[88:91], v[160:163], v[178:181], v[88:91]
	v_mfma_i32_16x16x64_i8 v[84:87], v[152:155], v[212:215], v[84:87]
	v_mfma_i32_16x16x64_i8 v[80:83], v[160:163], v[212:215], v[80:83]
	v_mfma_i32_16x16x64_i8 v[76:79], v[152:155], v[224:227], v[76:79]
	v_mfma_i32_16x16x64_i8 v[72:75], v[160:163], v[224:227], v[72:75]
	v_mfma_i32_16x16x64_i8 v[68:71], v[152:155], v[232:235], v[68:71]
	v_mfma_i32_16x16x64_i8 v[64:67], v[160:163], v[232:235], v[64:67]
	s_barrier
	s_mov_b32 m0, s26
	ds_read_b128 v[174:177], v207 offset:16384
	ds_read_b128 v[178:181], v207 offset:17408
	ds_read_b128 v[208:211], v207 offset:18432
	ds_read_b128 v[212:215], v207 offset:19456
	ds_read_b128 v[216:219], v207 offset:20480
	ds_read_b128 v[224:227], v207 offset:21504
	ds_read_b128 v[228:231], v207 offset:22528
	ds_read_b128 v[232:235], v207 offset:23552
	buffer_load_dwordx4 v167, s[56:59], s8 offen lds
	s_mov_b32 m0, s27
	s_add_i32 s12, s8, 0x40000
	buffer_load_dwordx4 v183, s[56:59], s8 offen lds
	s_mov_b32 m0, s28
	s_nop 0
	buffer_load_dwordx4 v167, s[56:59], s12 offen lds
	s_mov_b32 m0, s29
	s_nop 0
	buffer_load_dwordx4 v183, s[56:59], s12 offen lds
	s_mov_b32 m0, s25
	s_nop 0
	buffer_load_dwordx4 v166, s[56:59], s9 offen lds
	s_mov_b32 m0, s30
	s_nop 0
	buffer_load_dwordx4 v182, s[56:59], s9 offen lds
	s_waitcnt vmcnt(8)
	s_waitcnt lgkmcnt(0)
	s_barrier
	s_waitcnt lgkmcnt(7)
	v_mfma_i32_16x16x64_i8 v[60:63], v[132:135], v[174:177], v[60:63]
	v_mfma_i32_16x16x64_i8 v[56:59], v[140:143], v[174:177], v[56:59]
	s_waitcnt lgkmcnt(5)
	v_mfma_i32_16x16x64_i8 v[52:55], v[132:135], v[208:211], v[52:55]
	v_mfma_i32_16x16x64_i8 v[48:51], v[140:143], v[208:211], v[48:51]
	s_waitcnt lgkmcnt(3)
	v_mfma_i32_16x16x64_i8 v[44:47], v[132:135], v[216:219], v[44:47]
	v_mfma_i32_16x16x64_i8 v[40:43], v[140:143], v[216:219], v[40:43]
	s_waitcnt lgkmcnt(1)
	v_mfma_i32_16x16x64_i8 v[36:39], v[132:135], v[228:231], v[36:39]
	v_mfma_i32_16x16x64_i8 v[32:35], v[140:143], v[228:231], v[32:35]
	v_mfma_i32_16x16x64_i8 v[60:63], v[136:139], v[178:181], v[60:63]
	v_mfma_i32_16x16x64_i8 v[56:59], v[144:147], v[178:181], v[56:59]
	v_mfma_i32_16x16x64_i8 v[52:55], v[136:139], v[212:215], v[52:55]
	v_mfma_i32_16x16x64_i8 v[48:51], v[144:147], v[212:215], v[48:51]
	v_mfma_i32_16x16x64_i8 v[44:47], v[136:139], v[224:227], v[44:47]
	v_mfma_i32_16x16x64_i8 v[40:43], v[144:147], v[224:227], v[40:43]
	s_waitcnt lgkmcnt(0)
	v_mfma_i32_16x16x64_i8 v[36:39], v[136:139], v[232:235], v[36:39]
	v_mfma_i32_16x16x64_i8 v[32:35], v[144:147], v[232:235], v[32:35]
	v_mfma_i32_16x16x64_i8 v[28:31], v[148:151], v[174:177], v[28:31]
	v_mfma_i32_16x16x64_i8 v[24:27], v[156:159], v[174:177], v[24:27]
	v_mfma_i32_16x16x64_i8 v[20:23], v[148:151], v[208:211], v[20:23]
	v_mfma_i32_16x16x64_i8 v[16:19], v[156:159], v[208:211], v[16:19]
	v_mfma_i32_16x16x64_i8 v[12:15], v[148:151], v[216:219], v[12:15]
	v_mfma_i32_16x16x64_i8 v[8:11], v[156:159], v[216:219], v[8:11]
	v_mfma_i32_16x16x64_i8 v[4:7], v[148:151], v[228:231], v[4:7]
	v_mfma_i32_16x16x64_i8 v[0:3], v[156:159], v[228:231], v[0:3]
	v_mfma_i32_16x16x64_i8 v[28:31], v[152:155], v[178:181], v[28:31]
	v_mfma_i32_16x16x64_i8 v[24:27], v[160:163], v[178:181], v[24:27]
	v_mfma_i32_16x16x64_i8 v[20:23], v[152:155], v[212:215], v[20:23]
	v_mfma_i32_16x16x64_i8 v[16:19], v[160:163], v[212:215], v[16:19]
	v_mfma_i32_16x16x64_i8 v[12:15], v[152:155], v[224:227], v[12:15]
	v_mfma_i32_16x16x64_i8 v[8:11], v[160:163], v[224:227], v[8:11]
	v_mfma_i32_16x16x64_i8 v[4:7], v[152:155], v[232:235], v[4:7]
	v_mfma_i32_16x16x64_i8 v[0:3], v[160:163], v[232:235], v[0:3]
	s_barrier
	ds_read_b128 v[132:135], v206 offset:32768
	ds_read_b128 v[136:139], v206 offset:33792
	ds_read_b128 v[140:143], v206 offset:34816
	ds_read_b128 v[144:147], v206 offset:35840
	ds_read_b128 v[148:151], v206 offset:49152
	ds_read_b128 v[152:155], v206 offset:50176
	ds_read_b128 v[156:159], v206 offset:51200
	ds_read_b128 v[160:163], v206 offset:52224
	s_add_i32 s9, s9, 0x40000
	s_mov_b32 m0, s31
	ds_read_b128 v[174:177], v207 offset:32768
	ds_read_b128 v[178:181], v207 offset:33792
	ds_read_b128 v[208:211], v207 offset:34816
	ds_read_b128 v[212:215], v207 offset:35840
	ds_read_b128 v[216:219], v207 offset:36864
	ds_read_b128 v[224:227], v207 offset:37888
	ds_read_b128 v[228:231], v207 offset:38912
	ds_read_b128 v[232:235], v207 offset:39936
	buffer_load_dwordx4 v166, s[56:59], s9 offen lds
	s_mov_b32 m0, s33
	s_nop 0
	buffer_load_dwordx4 v182, s[56:59], s9 offen lds
	s_waitcnt vmcnt(8)
	s_waitcnt lgkmcnt(0)
	s_barrier
	s_waitcnt lgkmcnt(7)
	v_mfma_i32_16x16x64_i8 v[124:127], v[132:135], v[174:177], v[124:127]
	v_mfma_i32_16x16x64_i8 v[120:123], v[140:143], v[174:177], v[120:123]
	s_waitcnt lgkmcnt(5)
	v_mfma_i32_16x16x64_i8 v[116:119], v[132:135], v[208:211], v[116:119]
	v_mfma_i32_16x16x64_i8 v[112:115], v[140:143], v[208:211], v[112:115]
	s_waitcnt lgkmcnt(3)
	v_mfma_i32_16x16x64_i8 v[108:111], v[132:135], v[216:219], v[108:111]
	v_mfma_i32_16x16x64_i8 v[104:107], v[140:143], v[216:219], v[104:107]
	s_waitcnt lgkmcnt(1)
	v_mfma_i32_16x16x64_i8 v[100:103], v[132:135], v[228:231], v[100:103]
	v_mfma_i32_16x16x64_i8 v[96:99], v[140:143], v[228:231], v[96:99]
	v_mfma_i32_16x16x64_i8 v[124:127], v[136:139], v[178:181], v[124:127]
	v_mfma_i32_16x16x64_i8 v[120:123], v[144:147], v[178:181], v[120:123]
	v_mfma_i32_16x16x64_i8 v[116:119], v[136:139], v[212:215], v[116:119]
	v_mfma_i32_16x16x64_i8 v[112:115], v[144:147], v[212:215], v[112:115]
	v_mfma_i32_16x16x64_i8 v[108:111], v[136:139], v[224:227], v[108:111]
	v_mfma_i32_16x16x64_i8 v[104:107], v[144:147], v[224:227], v[104:107]
	s_waitcnt lgkmcnt(0)
	v_mfma_i32_16x16x64_i8 v[100:103], v[136:139], v[232:235], v[100:103]
	v_mfma_i32_16x16x64_i8 v[96:99], v[144:147], v[232:235], v[96:99]
	v_mfma_i32_16x16x64_i8 v[92:95], v[148:151], v[174:177], v[92:95]
	v_mfma_i32_16x16x64_i8 v[88:91], v[156:159], v[174:177], v[88:91]
	v_mfma_i32_16x16x64_i8 v[84:87], v[148:151], v[208:211], v[84:87]
	v_mfma_i32_16x16x64_i8 v[80:83], v[156:159], v[208:211], v[80:83]
	v_mfma_i32_16x16x64_i8 v[76:79], v[148:151], v[216:219], v[76:79]
	v_mfma_i32_16x16x64_i8 v[72:75], v[156:159], v[216:219], v[72:75]
	v_mfma_i32_16x16x64_i8 v[68:71], v[148:151], v[228:231], v[68:71]
	v_mfma_i32_16x16x64_i8 v[64:67], v[156:159], v[228:231], v[64:67]
	v_mfma_i32_16x16x64_i8 v[92:95], v[152:155], v[178:181], v[92:95]
	v_mfma_i32_16x16x64_i8 v[88:91], v[160:163], v[178:181], v[88:91]
	v_mfma_i32_16x16x64_i8 v[84:87], v[152:155], v[212:215], v[84:87]
	v_mfma_i32_16x16x64_i8 v[80:83], v[160:163], v[212:215], v[80:83]
	v_mfma_i32_16x16x64_i8 v[76:79], v[152:155], v[224:227], v[76:79]
	v_mfma_i32_16x16x64_i8 v[72:75], v[160:163], v[224:227], v[72:75]
	v_mfma_i32_16x16x64_i8 v[68:71], v[152:155], v[232:235], v[68:71]
	v_mfma_i32_16x16x64_i8 v[64:67], v[160:163], v[232:235], v[64:67]
	s_barrier
	s_mov_b32 m0, s61
	s_add_i32 s9, s8, 0x80
	ds_read_b128 v[174:177], v207 offset:49152
	ds_read_b128 v[178:181], v207 offset:50176
	ds_read_b128 v[208:211], v207 offset:51200
	ds_read_b128 v[212:215], v207 offset:52224
	ds_read_b128 v[216:219], v207 offset:53248
	ds_read_b128 v[224:227], v207 offset:54272
	ds_read_b128 v[228:231], v207 offset:55296
	ds_read_b128 v[232:235], v207 offset:56320
	buffer_load_dwordx4 v167, s[56:59], s9 offen lds
	s_mov_b32 m0, s62
	s_add_i32 s8, s8, 0x40080
	buffer_load_dwordx4 v183, s[56:59], s9 offen lds
	s_mov_b32 m0, s52
	s_nop 0
	buffer_load_dwordx4 v167, s[56:59], s8 offen lds
	s_mov_b32 m0, s53
	s_nop 0
	buffer_load_dwordx4 v183, s[56:59], s8 offen lds
	s_mov_b32 m0, s63
	s_nop 0
	buffer_load_dwordx4 v166, s[56:59], s3 offen lds
	s_mov_b32 m0, s64
	s_nop 0
	buffer_load_dwordx4 v182, s[56:59], s3 offen lds
	s_waitcnt vmcnt(8)
	s_waitcnt lgkmcnt(0)
	s_barrier
	s_waitcnt lgkmcnt(7)
	v_mfma_i32_16x16x64_i8 v[60:63], v[132:135], v[174:177], v[60:63]
	v_mfma_i32_16x16x64_i8 v[56:59], v[140:143], v[174:177], v[56:59]
	s_waitcnt lgkmcnt(5)
	v_mfma_i32_16x16x64_i8 v[52:55], v[132:135], v[208:211], v[52:55]
	v_mfma_i32_16x16x64_i8 v[48:51], v[140:143], v[208:211], v[48:51]
	s_waitcnt lgkmcnt(3)
	v_mfma_i32_16x16x64_i8 v[44:47], v[132:135], v[216:219], v[44:47]
	v_mfma_i32_16x16x64_i8 v[40:43], v[140:143], v[216:219], v[40:43]
	s_waitcnt lgkmcnt(1)
	v_mfma_i32_16x16x64_i8 v[36:39], v[132:135], v[228:231], v[36:39]
	v_mfma_i32_16x16x64_i8 v[32:35], v[140:143], v[228:231], v[32:35]
	v_mfma_i32_16x16x64_i8 v[60:63], v[136:139], v[178:181], v[60:63]
	v_mfma_i32_16x16x64_i8 v[56:59], v[144:147], v[178:181], v[56:59]
	v_mfma_i32_16x16x64_i8 v[52:55], v[136:139], v[212:215], v[52:55]
	v_mfma_i32_16x16x64_i8 v[48:51], v[144:147], v[212:215], v[48:51]
	v_mfma_i32_16x16x64_i8 v[44:47], v[136:139], v[224:227], v[44:47]
	v_mfma_i32_16x16x64_i8 v[40:43], v[144:147], v[224:227], v[40:43]
	s_waitcnt lgkmcnt(0)
	v_mfma_i32_16x16x64_i8 v[36:39], v[136:139], v[232:235], v[36:39]
	v_mfma_i32_16x16x64_i8 v[32:35], v[144:147], v[232:235], v[32:35]
	v_mfma_i32_16x16x64_i8 v[28:31], v[148:151], v[174:177], v[28:31]
	v_mfma_i32_16x16x64_i8 v[24:27], v[156:159], v[174:177], v[24:27]
	v_mfma_i32_16x16x64_i8 v[20:23], v[148:151], v[208:211], v[20:23]
	v_mfma_i32_16x16x64_i8 v[16:19], v[156:159], v[208:211], v[16:19]
	v_mfma_i32_16x16x64_i8 v[12:15], v[148:151], v[216:219], v[12:15]
	v_mfma_i32_16x16x64_i8 v[8:11], v[156:159], v[216:219], v[8:11]
	v_mfma_i32_16x16x64_i8 v[4:7], v[148:151], v[228:231], v[4:7]
	v_mfma_i32_16x16x64_i8 v[0:3], v[156:159], v[228:231], v[0:3]
	v_mfma_i32_16x16x64_i8 v[28:31], v[152:155], v[178:181], v[28:31]
	v_mfma_i32_16x16x64_i8 v[24:27], v[160:163], v[178:181], v[24:27]
	v_mfma_i32_16x16x64_i8 v[20:23], v[152:155], v[212:215], v[20:23]
	v_mfma_i32_16x16x64_i8 v[16:19], v[160:163], v[212:215], v[16:19]
	v_mfma_i32_16x16x64_i8 v[12:15], v[152:155], v[224:227], v[12:15]
	v_mfma_i32_16x16x64_i8 v[8:11], v[160:163], v[224:227], v[8:11]
	v_mfma_i32_16x16x64_i8 v[4:7], v[152:155], v[232:235], v[4:7]
	v_mfma_i32_16x16x64_i8 v[0:3], v[160:163], v[232:235], v[0:3]
	s_barrier
	s_add_i32 s2, s2, 2
	s_addk_i32 s0, 0x100
	s_addk_i32 s1, 0x100
	s_cmp_gt_u32 s2, 13
	s_cbranch_scc0 .LBB0_242
	s_and_b64 vcc, exec, s[18:19]
	s_cbranch_vccz .LBB0_245
	s_barrier

.LBB0_710:
	ds_read_b128 v[130:133], v143
	ds_read_b128 v[146:149], v143 offset:1024
	ds_read_b128 v[150:153], v143 offset:2048
	ds_read_b128 v[154:157], v143 offset:3072
	ds_read_b128 v[164:167], v143 offset:16384
	ds_read_b128 v[174:177], v143 offset:17408
	ds_read_b128 v[178:181], v143 offset:18432
	ds_read_b128 v[182:185], v143 offset:19456
	s_add_i32 s13, s8, 0xfff00080
	s_cmp_eq_u32 s12, 60
	s_cselect_b32 s15, s53, s13
	s_cselect_b32 s14, s54, s9
	s_add_i32 s13, s15, 0x80
	s_mov_b32 s56, s78
	s_mov_b32 m0, s46
	ds_read_b128 v[198:201], v144
	ds_read_b128 v[202:205], v144 offset:1024
	ds_read_b128 v[206:209], v144 offset:2048
	ds_read_b128 v[210:213], v144 offset:3072
	ds_read_b128 v[214:217], v144 offset:4096
	ds_read_b128 v[224:227], v144 offset:5120
	ds_read_b128 v[228:231], v144 offset:6144
	ds_read_b128 v[232:235], v144 offset:7168
	buffer_load_dwordx4 v129, s[56:59], s8 offen lds
	s_mov_b32 m0, s48
	s_nop 0
	buffer_load_dwordx4 v137, s[56:59], s8 offen lds
	s_waitcnt vmcnt(8)
	s_waitcnt lgkmcnt(0)
	s_barrier
	s_waitcnt lgkmcnt(7)
	v_mfma_f32_16x16x32_bf16 v[124:127], v[130:133], v[198:201], v[124:127]
	v_mfma_f32_16x16x32_bf16 v[120:123], v[150:153], v[198:201], v[120:123]
	s_waitcnt lgkmcnt(5)
	v_mfma_f32_16x16x32_bf16 v[108:111], v[130:133], v[206:209], v[108:111]
	v_mfma_f32_16x16x32_bf16 v[104:107], v[150:153], v[206:209], v[104:107]
	s_waitcnt lgkmcnt(3)
	v_mfma_f32_16x16x32_bf16 v[92:95], v[130:133], v[214:217], v[92:95]
	v_mfma_f32_16x16x32_bf16 v[88:91], v[150:153], v[214:217], v[88:91]
	s_waitcnt lgkmcnt(1)
	v_mfma_f32_16x16x32_bf16 v[76:79], v[130:133], v[228:231], v[76:79]
	v_mfma_f32_16x16x32_bf16 v[72:75], v[150:153], v[228:231], v[72:75]
	v_mfma_f32_16x16x32_bf16 v[124:127], v[146:149], v[202:205], v[124:127]
	v_mfma_f32_16x16x32_bf16 v[120:123], v[154:157], v[202:205], v[120:123]
	v_mfma_f32_16x16x32_bf16 v[108:111], v[146:149], v[210:213], v[108:111]
	v_mfma_f32_16x16x32_bf16 v[104:107], v[154:157], v[210:213], v[104:107]
	v_mfma_f32_16x16x32_bf16 v[92:95], v[146:149], v[224:227], v[92:95]
	v_mfma_f32_16x16x32_bf16 v[88:91], v[154:157], v[224:227], v[88:91]
	s_waitcnt lgkmcnt(0)
	v_mfma_f32_16x16x32_bf16 v[76:79], v[146:149], v[232:235], v[76:79]
	v_mfma_f32_16x16x32_bf16 v[72:75], v[154:157], v[232:235], v[72:75]
	v_mfma_f32_16x16x32_bf16 v[116:119], v[164:167], v[198:201], v[116:119]
	v_mfma_f32_16x16x32_bf16 v[112:115], v[178:181], v[198:201], v[112:115]
	v_mfma_f32_16x16x32_bf16 v[100:103], v[164:167], v[206:209], v[100:103]
	v_mfma_f32_16x16x32_bf16 v[96:99], v[178:181], v[206:209], v[96:99]
	v_mfma_f32_16x16x32_bf16 v[84:87], v[164:167], v[214:217], v[84:87]
	v_mfma_f32_16x16x32_bf16 v[80:83], v[178:181], v[214:217], v[80:83]
	v_mfma_f32_16x16x32_bf16 v[68:71], v[164:167], v[228:231], v[68:71]
	v_mfma_f32_16x16x32_bf16 v[64:67], v[178:181], v[228:231], v[64:67]
	v_mfma_f32_16x16x32_bf16 v[116:119], v[174:177], v[202:205], v[116:119]
	v_mfma_f32_16x16x32_bf16 v[112:115], v[182:185], v[202:205], v[112:115]
	v_mfma_f32_16x16x32_bf16 v[100:103], v[174:177], v[210:213], v[100:103]
	v_mfma_f32_16x16x32_bf16 v[96:99], v[182:185], v[210:213], v[96:99]
	v_mfma_f32_16x16x32_bf16 v[84:87], v[174:177], v[224:227], v[84:87]
	v_mfma_f32_16x16x32_bf16 v[80:83], v[182:185], v[224:227], v[80:83]
	v_mfma_f32_16x16x32_bf16 v[68:71], v[174:177], v[232:235], v[68:71]
	v_mfma_f32_16x16x32_bf16 v[64:67], v[182:185], v[232:235], v[64:67]
	s_barrier
	s_mov_b32 m0, s21
	ds_read_b128 v[198:201], v144 offset:16384
	ds_read_b128 v[202:205], v144 offset:17408
	ds_read_b128 v[206:209], v144 offset:18432
	ds_read_b128 v[210:213], v144 offset:19456
	ds_read_b128 v[214:217], v144 offset:20480
	ds_read_b128 v[224:227], v144 offset:21504
	ds_read_b128 v[228:231], v144 offset:22528
	ds_read_b128 v[232:235], v144 offset:23552
	buffer_load_dwordx4 v136, s[56:59], s14 offen lds
	s_mov_b32 m0, s22
	s_add_i32 s33, s14, 0x100000
	buffer_load_dwordx4 v138, s[56:59], s14 offen lds
	s_mov_b32 m0, s23
	s_nop 0
	buffer_load_dwordx4 v136, s[56:59], s33 offen lds
	s_mov_b32 m0, s24
	s_nop 0
	buffer_load_dwordx4 v138, s[56:59], s33 offen lds
	s_mov_b32 m0, s20
	s_nop 0
	buffer_load_dwordx4 v129, s[56:59], s15 offen lds
	s_mov_b32 m0, s25
	s_nop 0
	buffer_load_dwordx4 v137, s[56:59], s15 offen lds
	s_waitcnt vmcnt(8)
	s_waitcnt lgkmcnt(0)
	s_barrier
	s_waitcnt lgkmcnt(7)
	v_mfma_f32_16x16x32_bf16 v[60:63], v[130:133], v[198:201], v[60:63]
	v_mfma_f32_16x16x32_bf16 v[56:59], v[150:153], v[198:201], v[56:59]
	s_waitcnt lgkmcnt(5)
	v_mfma_f32_16x16x32_bf16 v[44:47], v[130:133], v[206:209], v[44:47]
	v_mfma_f32_16x16x32_bf16 v[40:43], v[150:153], v[206:209], v[40:43]
	s_waitcnt lgkmcnt(3)
	v_mfma_f32_16x16x32_bf16 v[28:31], v[130:133], v[214:217], v[28:31]
	v_mfma_f32_16x16x32_bf16 v[24:27], v[150:153], v[214:217], v[24:27]
	s_waitcnt lgkmcnt(1)
	v_mfma_f32_16x16x32_bf16 v[12:15], v[130:133], v[228:231], v[12:15]
	v_mfma_f32_16x16x32_bf16 v[8:11], v[150:153], v[228:231], v[8:11]
	v_mfma_f32_16x16x32_bf16 v[60:63], v[146:149], v[202:205], v[60:63]
	v_mfma_f32_16x16x32_bf16 v[56:59], v[154:157], v[202:205], v[56:59]
	v_mfma_f32_16x16x32_bf16 v[44:47], v[146:149], v[210:213], v[44:47]
	v_mfma_f32_16x16x32_bf16 v[40:43], v[154:157], v[210:213], v[40:43]
	v_mfma_f32_16x16x32_bf16 v[28:31], v[146:149], v[224:227], v[28:31]
	v_mfma_f32_16x16x32_bf16 v[24:27], v[154:157], v[224:227], v[24:27]
	s_waitcnt lgkmcnt(0)
	v_mfma_f32_16x16x32_bf16 v[12:15], v[146:149], v[232:235], v[12:15]
	v_mfma_f32_16x16x32_bf16 v[8:11], v[154:157], v[232:235], v[8:11]
	v_mfma_f32_16x16x32_bf16 v[52:55], v[164:167], v[198:201], v[52:55]
	v_mfma_f32_16x16x32_bf16 v[48:51], v[178:181], v[198:201], v[48:51]
	v_mfma_f32_16x16x32_bf16 v[36:39], v[164:167], v[206:209], v[36:39]
	v_mfma_f32_16x16x32_bf16 v[32:35], v[178:181], v[206:209], v[32:35]
	v_mfma_f32_16x16x32_bf16 v[20:23], v[164:167], v[214:217], v[20:23]
	v_mfma_f32_16x16x32_bf16 v[16:19], v[178:181], v[214:217], v[16:19]
	v_mfma_f32_16x16x32_bf16 v[4:7], v[164:167], v[228:231], v[4:7]
	v_mfma_f32_16x16x32_bf16 v[0:3], v[178:181], v[228:231], v[0:3]
	v_mfma_f32_16x16x32_bf16 v[52:55], v[174:177], v[202:205], v[52:55]
	v_mfma_f32_16x16x32_bf16 v[48:51], v[182:185], v[202:205], v[48:51]
	v_mfma_f32_16x16x32_bf16 v[36:39], v[174:177], v[210:213], v[36:39]
	v_mfma_f32_16x16x32_bf16 v[32:35], v[182:185], v[210:213], v[32:35]
	v_mfma_f32_16x16x32_bf16 v[20:23], v[174:177], v[224:227], v[20:23]
	v_mfma_f32_16x16x32_bf16 v[16:19], v[182:185], v[224:227], v[16:19]
	v_mfma_f32_16x16x32_bf16 v[4:7], v[174:177], v[232:235], v[4:7]
	v_mfma_f32_16x16x32_bf16 v[0:3], v[182:185], v[232:235], v[0:3]
	s_barrier
	ds_read_b128 v[130:133], v143 offset:32768
	ds_read_b128 v[146:149], v143 offset:33792
	ds_read_b128 v[150:153], v143 offset:34816
	ds_read_b128 v[154:157], v143 offset:35840
	ds_read_b128 v[164:167], v143 offset:49152
	ds_read_b128 v[174:177], v143 offset:50176
	ds_read_b128 v[178:181], v143 offset:51200
	ds_read_b128 v[182:185], v143 offset:52224
	s_add_i32 s15, s15, 0x100000
	s_mov_b32 m0, s26
	ds_read_b128 v[198:201], v144 offset:32768
	ds_read_b128 v[202:205], v144 offset:33792
	ds_read_b128 v[206:209], v144 offset:34816
	ds_read_b128 v[210:213], v144 offset:35840
	ds_read_b128 v[214:217], v144 offset:36864
	ds_read_b128 v[224:227], v144 offset:37888
	ds_read_b128 v[228:231], v144 offset:38912
	ds_read_b128 v[232:235], v144 offset:39936
	buffer_load_dwordx4 v129, s[56:59], s15 offen lds
	s_mov_b32 m0, s27
	s_nop 0
	buffer_load_dwordx4 v137, s[56:59], s15 offen lds
	s_waitcnt vmcnt(8)
	s_waitcnt lgkmcnt(0)
	s_barrier
	s_waitcnt lgkmcnt(7)
	v_mfma_f32_16x16x32_bf16 v[124:127], v[130:133], v[198:201], v[124:127]
	v_mfma_f32_16x16x32_bf16 v[120:123], v[150:153], v[198:201], v[120:123]
	s_waitcnt lgkmcnt(5)
	v_mfma_f32_16x16x32_bf16 v[108:111], v[130:133], v[206:209], v[108:111]
	v_mfma_f32_16x16x32_bf16 v[104:107], v[150:153], v[206:209], v[104:107]
	s_waitcnt lgkmcnt(3)
	v_mfma_f32_16x16x32_bf16 v[92:95], v[130:133], v[214:217], v[92:95]
	v_mfma_f32_16x16x32_bf16 v[88:91], v[150:153], v[214:217], v[88:91]
	s_waitcnt lgkmcnt(1)
	v_mfma_f32_16x16x32_bf16 v[76:79], v[130:133], v[228:231], v[76:79]
	v_mfma_f32_16x16x32_bf16 v[72:75], v[150:153], v[228:231], v[72:75]
	v_mfma_f32_16x16x32_bf16 v[124:127], v[146:149], v[202:205], v[124:127]
	v_mfma_f32_16x16x32_bf16 v[120:123], v[154:157], v[202:205], v[120:123]
	v_mfma_f32_16x16x32_bf16 v[108:111], v[146:149], v[210:213], v[108:111]
	v_mfma_f32_16x16x32_bf16 v[104:107], v[154:157], v[210:213], v[104:107]
	v_mfma_f32_16x16x32_bf16 v[92:95], v[146:149], v[224:227], v[92:95]
	v_mfma_f32_16x16x32_bf16 v[88:91], v[154:157], v[224:227], v[88:91]
	s_waitcnt lgkmcnt(0)
	v_mfma_f32_16x16x32_bf16 v[76:79], v[146:149], v[232:235], v[76:79]
	v_mfma_f32_16x16x32_bf16 v[72:75], v[154:157], v[232:235], v[72:75]
	v_mfma_f32_16x16x32_bf16 v[116:119], v[164:167], v[198:201], v[116:119]
	v_mfma_f32_16x16x32_bf16 v[112:115], v[178:181], v[198:201], v[112:115]
	v_mfma_f32_16x16x32_bf16 v[100:103], v[164:167], v[206:209], v[100:103]
	v_mfma_f32_16x16x32_bf16 v[96:99], v[178:181], v[206:209], v[96:99]
	v_mfma_f32_16x16x32_bf16 v[84:87], v[164:167], v[214:217], v[84:87]
	v_mfma_f32_16x16x32_bf16 v[80:83], v[178:181], v[214:217], v[80:83]
	v_mfma_f32_16x16x32_bf16 v[68:71], v[164:167], v[228:231], v[68:71]
	v_mfma_f32_16x16x32_bf16 v[64:67], v[178:181], v[228:231], v[64:67]
	v_mfma_f32_16x16x32_bf16 v[116:119], v[174:177], v[202:205], v[116:119]
	v_mfma_f32_16x16x32_bf16 v[112:115], v[182:185], v[202:205], v[112:115]
	v_mfma_f32_16x16x32_bf16 v[100:103], v[174:177], v[210:213], v[100:103]
	v_mfma_f32_16x16x32_bf16 v[96:99], v[182:185], v[210:213], v[96:99]
	v_mfma_f32_16x16x32_bf16 v[84:87], v[174:177], v[224:227], v[84:87]
	v_mfma_f32_16x16x32_bf16 v[80:83], v[182:185], v[224:227], v[80:83]
	v_mfma_f32_16x16x32_bf16 v[68:71], v[174:177], v[232:235], v[68:71]
	v_mfma_f32_16x16x32_bf16 v[64:67], v[182:185], v[232:235], v[64:67]
	s_barrier
	s_mov_b32 m0, s29
	s_add_i32 s15, s14, 0x80
	ds_read_b128 v[198:201], v144 offset:49152
	ds_read_b128 v[202:205], v144 offset:50176
	ds_read_b128 v[206:209], v144 offset:51200
	ds_read_b128 v[210:213], v144 offset:52224
	ds_read_b128 v[214:217], v144 offset:53248
	ds_read_b128 v[224:227], v144 offset:54272
	ds_read_b128 v[228:231], v144 offset:55296
	ds_read_b128 v[232:235], v144 offset:56320
	buffer_load_dwordx4 v136, s[56:59], s15 offen lds
	s_mov_b32 m0, s30
	s_add_i32 s14, s14, 0x100080
	buffer_load_dwordx4 v138, s[56:59], s15 offen lds
	s_mov_b32 m0, s37
	s_nop 0
	buffer_load_dwordx4 v136, s[56:59], s14 offen lds
	s_mov_b32 m0, s45
	s_nop 0
	buffer_load_dwordx4 v138, s[56:59], s14 offen lds
	s_mov_b32 m0, s31
	s_nop 0
	buffer_load_dwordx4 v129, s[56:59], s13 offen lds
	s_mov_b32 m0, s36
	s_nop 0
	buffer_load_dwordx4 v137, s[56:59], s13 offen lds
	s_waitcnt vmcnt(8)
	s_waitcnt lgkmcnt(0)
	s_barrier
	s_waitcnt lgkmcnt(7)
	v_mfma_f32_16x16x32_bf16 v[60:63], v[130:133], v[198:201], v[60:63]
	v_mfma_f32_16x16x32_bf16 v[56:59], v[150:153], v[198:201], v[56:59]
	s_waitcnt lgkmcnt(5)
	v_mfma_f32_16x16x32_bf16 v[44:47], v[130:133], v[206:209], v[44:47]
	v_mfma_f32_16x16x32_bf16 v[40:43], v[150:153], v[206:209], v[40:43]
	s_waitcnt lgkmcnt(3)
	v_mfma_f32_16x16x32_bf16 v[28:31], v[130:133], v[214:217], v[28:31]
	v_mfma_f32_16x16x32_bf16 v[24:27], v[150:153], v[214:217], v[24:27]
	s_waitcnt lgkmcnt(1)
	v_mfma_f32_16x16x32_bf16 v[12:15], v[130:133], v[228:231], v[12:15]
	v_mfma_f32_16x16x32_bf16 v[8:11], v[150:153], v[228:231], v[8:11]
	v_mfma_f32_16x16x32_bf16 v[60:63], v[146:149], v[202:205], v[60:63]
	v_mfma_f32_16x16x32_bf16 v[56:59], v[154:157], v[202:205], v[56:59]
	v_mfma_f32_16x16x32_bf16 v[44:47], v[146:149], v[210:213], v[44:47]
	v_mfma_f32_16x16x32_bf16 v[40:43], v[154:157], v[210:213], v[40:43]
	v_mfma_f32_16x16x32_bf16 v[28:31], v[146:149], v[224:227], v[28:31]
	v_mfma_f32_16x16x32_bf16 v[24:27], v[154:157], v[224:227], v[24:27]
	s_waitcnt lgkmcnt(0)
	v_mfma_f32_16x16x32_bf16 v[12:15], v[146:149], v[232:235], v[12:15]
	v_mfma_f32_16x16x32_bf16 v[8:11], v[154:157], v[232:235], v[8:11]
	v_mfma_f32_16x16x32_bf16 v[52:55], v[164:167], v[198:201], v[52:55]
	v_mfma_f32_16x16x32_bf16 v[48:51], v[178:181], v[198:201], v[48:51]
	v_mfma_f32_16x16x32_bf16 v[36:39], v[164:167], v[206:209], v[36:39]
	v_mfma_f32_16x16x32_bf16 v[32:35], v[178:181], v[206:209], v[32:35]
	v_mfma_f32_16x16x32_bf16 v[20:23], v[164:167], v[214:217], v[20:23]
	v_mfma_f32_16x16x32_bf16 v[16:19], v[178:181], v[214:217], v[16:19]
	v_mfma_f32_16x16x32_bf16 v[4:7], v[164:167], v[228:231], v[4:7]
	v_mfma_f32_16x16x32_bf16 v[0:3], v[178:181], v[228:231], v[0:3]
	v_mfma_f32_16x16x32_bf16 v[52:55], v[174:177], v[202:205], v[52:55]
	v_mfma_f32_16x16x32_bf16 v[48:51], v[182:185], v[202:205], v[48:51]
	v_mfma_f32_16x16x32_bf16 v[36:39], v[174:177], v[210:213], v[36:39]
	v_mfma_f32_16x16x32_bf16 v[32:35], v[182:185], v[210:213], v[32:35]
	v_mfma_f32_16x16x32_bf16 v[20:23], v[174:177], v[224:227], v[20:23]
	v_mfma_f32_16x16x32_bf16 v[16:19], v[182:185], v[224:227], v[16:19]
	v_mfma_f32_16x16x32_bf16 v[4:7], v[174:177], v[232:235], v[4:7]
	v_mfma_f32_16x16x32_bf16 v[0:3], v[182:185], v[232:235], v[0:3]
	s_barrier
	s_add_i32 s12, s12, 2
	s_addk_i32 s8, 0x100
	s_addk_i32 s9, 0x100
	s_cmp_gt_u32 s12, 61
	s_cbranch_scc0 .LBB0_710
	s_and_b64 vcc, exec, s[2:3]
	s_cbranch_vccz .LBB0_713
	s_barrier

.LBB0_782:
	ds_read_b128 v[16:19], v186
	ds_read_b128 v[20:23], v186 offset:1024
	ds_read_b128 v[24:27], v186 offset:2048
	ds_read_b128 v[28:31], v186 offset:3072
	s_waitcnt lgkmcnt(4)
	ds_read_b128 v[0:3], v186 offset:16384
	ds_read_b128 v[4:7], v186 offset:17408
	ds_read_b128 v[8:11], v186 offset:18432
	ds_read_b128 v[12:15], v186 offset:19456
	s_add_i32 s13, s8, 0xfff80080
	s_cmp_eq_u32 s12, 28
	s_cselect_b32 s15, s52, s13
	s_cselect_b32 s14, s53, s9
	s_add_i32 s13, s15, 0x80
	s_mov_b32 s56, s78
	s_mov_b32 m0, s45
	ds_read_b128 v[174:177], v198
	ds_read_b128 v[178:181], v198 offset:1024
	ds_read_b128 v[200:203], v198 offset:2048
	ds_read_b128 v[204:207], v198 offset:3072
	ds_read_b128 v[208:211], v198 offset:4096
	ds_read_b128 v[212:215], v198 offset:5120
	ds_read_b128 v[224:227], v198 offset:6144
	ds_read_b128 v[228:231], v198 offset:7168
	buffer_load_dwordx4 v165, s[56:59], s8 offen lds
	s_mov_b32 m0, s47
	s_nop 0
	buffer_load_dwordx4 v167, s[56:59], s8 offen lds
	s_waitcnt vmcnt(8)
	s_waitcnt lgkmcnt(0)
	s_barrier
	s_waitcnt lgkmcnt(6)
	v_mfma_f32_16x16x128_f8f6f4 v[156:159], v[16:23], v[174:181], v[156:159]
	v_mfma_f32_16x16x128_f8f6f4 v[152:155], v[24:31], v[174:181], v[152:155]
	s_waitcnt lgkmcnt(4)
	v_mfma_f32_16x16x128_f8f6f4 v[140:143], v[16:23], v[200:207], v[140:143]
	v_mfma_f32_16x16x128_f8f6f4 v[136:139], v[24:31], v[200:207], v[136:139]
	s_waitcnt lgkmcnt(2)
	v_mfma_f32_16x16x128_f8f6f4 v[124:127], v[16:23], v[208:215], v[124:127]
	v_mfma_f32_16x16x128_f8f6f4 v[120:123], v[24:31], v[208:215], v[120:123]
	s_waitcnt lgkmcnt(0)
	v_mfma_f32_16x16x128_f8f6f4 v[108:111], v[16:23], v[224:231], v[108:111]
	v_mfma_f32_16x16x128_f8f6f4 v[104:107], v[24:31], v[224:231], v[104:107]
	v_mfma_f32_16x16x128_f8f6f4 v[148:151], v[0:7], v[174:181], v[148:151]
	v_mfma_f32_16x16x128_f8f6f4 v[144:147], v[8:15], v[174:181], v[144:147]
	v_mfma_f32_16x16x128_f8f6f4 v[132:135], v[0:7], v[200:207], v[132:135]
	v_mfma_f32_16x16x128_f8f6f4 v[128:131], v[8:15], v[200:207], v[128:131]
	v_mfma_f32_16x16x128_f8f6f4 v[116:119], v[0:7], v[208:215], v[116:119]
	v_mfma_f32_16x16x128_f8f6f4 v[112:115], v[8:15], v[208:215], v[112:115]
	v_mfma_f32_16x16x128_f8f6f4 v[100:103], v[0:7], v[224:231], v[100:103]
	v_mfma_f32_16x16x128_f8f6f4 v[96:99], v[8:15], v[224:231], v[96:99]
	s_barrier
	s_mov_b32 m0, s21
	ds_read_b128 v[174:177], v198 offset:16384
	ds_read_b128 v[178:181], v198 offset:17408
	ds_read_b128 v[200:203], v198 offset:18432
	ds_read_b128 v[204:207], v198 offset:19456
	ds_read_b128 v[208:211], v198 offset:20480
	ds_read_b128 v[212:215], v198 offset:21504
	ds_read_b128 v[224:227], v198 offset:22528
	ds_read_b128 v[228:231], v198 offset:23552
	buffer_load_dwordx4 v166, s[56:59], s14 offen lds
	s_mov_b32 m0, s22
	s_add_i32 s33, s14, 0x80000
	buffer_load_dwordx4 v172, s[56:59], s14 offen lds
	s_mov_b32 m0, s23
	s_nop 0
	buffer_load_dwordx4 v166, s[56:59], s33 offen lds
	s_mov_b32 m0, s24
	s_nop 0
	buffer_load_dwordx4 v172, s[56:59], s33 offen lds
	s_mov_b32 m0, s20
	s_nop 0
	buffer_load_dwordx4 v165, s[56:59], s15 offen lds
	s_mov_b32 m0, s25
	s_nop 0
	buffer_load_dwordx4 v167, s[56:59], s15 offen lds
	s_waitcnt vmcnt(8)
	s_waitcnt lgkmcnt(0)
	s_barrier
	s_waitcnt lgkmcnt(6)
	v_mfma_f32_16x16x128_f8f6f4 v[92:95], v[16:23], v[174:181], v[92:95]
	v_mfma_f32_16x16x128_f8f6f4 v[88:91], v[24:31], v[174:181], v[88:91]
	s_waitcnt lgkmcnt(4)
	v_mfma_f32_16x16x128_f8f6f4 v[76:79], v[16:23], v[200:207], v[76:79]
	v_mfma_f32_16x16x128_f8f6f4 v[72:75], v[24:31], v[200:207], v[72:75]
	s_waitcnt lgkmcnt(2)
	v_mfma_f32_16x16x128_f8f6f4 v[60:63], v[16:23], v[208:215], v[60:63]
	v_mfma_f32_16x16x128_f8f6f4 v[56:59], v[24:31], v[208:215], v[56:59]
	s_waitcnt lgkmcnt(0)
	v_mfma_f32_16x16x128_f8f6f4 v[44:47], v[16:23], v[224:231], v[44:47]
	v_mfma_f32_16x16x128_f8f6f4 v[40:43], v[24:31], v[224:231], v[40:43]
	v_mfma_f32_16x16x128_f8f6f4 v[84:87], v[0:7], v[174:181], v[84:87]
	v_mfma_f32_16x16x128_f8f6f4 v[80:83], v[8:15], v[174:181], v[80:83]
	v_mfma_f32_16x16x128_f8f6f4 v[68:71], v[0:7], v[200:207], v[68:71]
	v_mfma_f32_16x16x128_f8f6f4 v[64:67], v[8:15], v[200:207], v[64:67]
	v_mfma_f32_16x16x128_f8f6f4 v[52:55], v[0:7], v[208:215], v[52:55]
	v_mfma_f32_16x16x128_f8f6f4 v[48:51], v[8:15], v[208:215], v[48:51]
	v_mfma_f32_16x16x128_f8f6f4 v[36:39], v[0:7], v[224:231], v[36:39]
	v_mfma_f32_16x16x128_f8f6f4 v[32:35], v[8:15], v[224:231], v[32:35]
	s_barrier
	ds_read_b128 v[0:3], v186 offset:32768
	ds_read_b128 v[4:7], v186 offset:33792
	ds_read_b128 v[8:11], v186 offset:34816
	ds_read_b128 v[12:15], v186 offset:35840
	ds_read_b128 v[16:19], v186 offset:49152
	ds_read_b128 v[20:23], v186 offset:50176
	ds_read_b128 v[24:27], v186 offset:51200
	ds_read_b128 v[28:31], v186 offset:52224
	s_add_i32 s15, s15, 0x80000
	s_mov_b32 m0, s26
	ds_read_b128 v[174:177], v198 offset:32768
	ds_read_b128 v[178:181], v198 offset:33792
	ds_read_b128 v[200:203], v198 offset:34816
	ds_read_b128 v[204:207], v198 offset:35840
	ds_read_b128 v[208:211], v198 offset:36864
	ds_read_b128 v[212:215], v198 offset:37888
	ds_read_b128 v[224:227], v198 offset:38912
	ds_read_b128 v[228:231], v198 offset:39936
	buffer_load_dwordx4 v165, s[56:59], s15 offen lds
	s_mov_b32 m0, s27
	s_nop 0
	buffer_load_dwordx4 v167, s[56:59], s15 offen lds
	s_waitcnt vmcnt(8)
	s_waitcnt lgkmcnt(0)
	s_barrier
	s_waitcnt lgkmcnt(6)
	v_mfma_f32_16x16x128_f8f6f4 v[156:159], v[0:7], v[174:181], v[156:159]
	v_mfma_f32_16x16x128_f8f6f4 v[152:155], v[8:15], v[174:181], v[152:155]
	s_waitcnt lgkmcnt(4)
	v_mfma_f32_16x16x128_f8f6f4 v[140:143], v[0:7], v[200:207], v[140:143]
	v_mfma_f32_16x16x128_f8f6f4 v[136:139], v[8:15], v[200:207], v[136:139]
	s_waitcnt lgkmcnt(2)
	v_mfma_f32_16x16x128_f8f6f4 v[124:127], v[0:7], v[208:215], v[124:127]
	v_mfma_f32_16x16x128_f8f6f4 v[120:123], v[8:15], v[208:215], v[120:123]
	s_waitcnt lgkmcnt(0)
	v_mfma_f32_16x16x128_f8f6f4 v[108:111], v[0:7], v[224:231], v[108:111]
	v_mfma_f32_16x16x128_f8f6f4 v[104:107], v[8:15], v[224:231], v[104:107]
	v_mfma_f32_16x16x128_f8f6f4 v[148:151], v[16:23], v[174:181], v[148:151]
	v_mfma_f32_16x16x128_f8f6f4 v[144:147], v[24:31], v[174:181], v[144:147]
	v_mfma_f32_16x16x128_f8f6f4 v[132:135], v[16:23], v[200:207], v[132:135]
	v_mfma_f32_16x16x128_f8f6f4 v[128:131], v[24:31], v[200:207], v[128:131]
	v_mfma_f32_16x16x128_f8f6f4 v[116:119], v[16:23], v[208:215], v[116:119]
	v_mfma_f32_16x16x128_f8f6f4 v[112:115], v[24:31], v[208:215], v[112:115]
	v_mfma_f32_16x16x128_f8f6f4 v[100:103], v[16:23], v[224:231], v[100:103]
	v_mfma_f32_16x16x128_f8f6f4 v[96:99], v[24:31], v[224:231], v[96:99]
	s_barrier
	s_mov_b32 m0, s28
	s_add_i32 s15, s14, 0x80
	ds_read_b128 v[174:177], v198 offset:49152
	ds_read_b128 v[178:181], v198 offset:50176
	ds_read_b128 v[200:203], v198 offset:51200
	ds_read_b128 v[204:207], v198 offset:52224
	ds_read_b128 v[208:211], v198 offset:53248
	ds_read_b128 v[212:215], v198 offset:54272
	ds_read_b128 v[224:227], v198 offset:55296
	ds_read_b128 v[228:231], v198 offset:56320
	buffer_load_dwordx4 v166, s[56:59], s15 offen lds
	s_mov_b32 m0, s29
	s_add_i32 s14, s14, 0x80080
	buffer_load_dwordx4 v172, s[56:59], s15 offen lds
	s_mov_b32 m0, s36
	s_nop 0
	buffer_load_dwordx4 v166, s[56:59], s14 offen lds
	s_mov_b32 m0, s37
	s_nop 0
	buffer_load_dwordx4 v172, s[56:59], s14 offen lds
	s_mov_b32 m0, s30
	s_nop 0
	buffer_load_dwordx4 v165, s[56:59], s13 offen lds
	s_mov_b32 m0, s31
	s_nop 0
	buffer_load_dwordx4 v167, s[56:59], s13 offen lds
	s_waitcnt vmcnt(8)
	s_waitcnt lgkmcnt(0)
	s_barrier
	s_waitcnt lgkmcnt(6)
	v_mfma_f32_16x16x128_f8f6f4 v[92:95], v[0:7], v[174:181], v[92:95]
	v_mfma_f32_16x16x128_f8f6f4 v[88:91], v[8:15], v[174:181], v[88:91]
	s_waitcnt lgkmcnt(4)
	v_mfma_f32_16x16x128_f8f6f4 v[76:79], v[0:7], v[200:207], v[76:79]
	v_mfma_f32_16x16x128_f8f6f4 v[72:75], v[8:15], v[200:207], v[72:75]
	s_waitcnt lgkmcnt(2)
	v_mfma_f32_16x16x128_f8f6f4 v[60:63], v[0:7], v[208:215], v[60:63]
	v_mfma_f32_16x16x128_f8f6f4 v[56:59], v[8:15], v[208:215], v[56:59]
	s_waitcnt lgkmcnt(0)
	v_mfma_f32_16x16x128_f8f6f4 v[44:47], v[0:7], v[224:231], v[44:47]
	v_mfma_f32_16x16x128_f8f6f4 v[40:43], v[8:15], v[224:231], v[40:43]
	v_mfma_f32_16x16x128_f8f6f4 v[84:87], v[16:23], v[174:181], v[84:87]
	v_mfma_f32_16x16x128_f8f6f4 v[80:83], v[24:31], v[174:181], v[80:83]
	v_mfma_f32_16x16x128_f8f6f4 v[68:71], v[16:23], v[200:207], v[68:71]
	v_mfma_f32_16x16x128_f8f6f4 v[64:67], v[24:31], v[200:207], v[64:67]
	v_mfma_f32_16x16x128_f8f6f4 v[52:55], v[16:23], v[208:215], v[52:55]
	v_mfma_f32_16x16x128_f8f6f4 v[48:51], v[24:31], v[208:215], v[48:51]
	v_mfma_f32_16x16x128_f8f6f4 v[36:39], v[16:23], v[224:231], v[36:39]
	v_mfma_f32_16x16x128_f8f6f4 v[32:35], v[24:31], v[224:231], v[32:35]
	s_barrier
	s_add_i32 s12, s12, 2
	s_addk_i32 s8, 0x100
	s_addk_i32 s9, 0x100
	s_cmp_gt_u32 s12, 29
	s_cbranch_scc0 .LBB0_782
	s_and_b64 vcc, exec, s[2:3]
	s_cbranch_vccz .LBB0_785
	s_barrier

.LBB0_965:
	ds_read_b128 v[130:133], v204
	ds_read_b128 v[134:137], v204 offset:1024
	ds_read_b128 v[138:141], v204 offset:2048
	ds_read_b128 v[144:147], v204 offset:3072
	ds_read_b128 v[148:151], v204 offset:16384
	ds_read_b128 v[152:155], v204 offset:17408
	ds_read_b128 v[156:159], v204 offset:18432
	ds_read_b128 v[162:165], v204 offset:19456
	s_add_i32 s15, s0, 0xfffc0080
	s_cmp_eq_u32 s14, 12
	s_cselect_b32 s49, s47, s15
	s_cselect_b32 s33, s48, s1
	s_add_i32 s15, s49, 0x80
	s_mov_b32 s56, s78
	s_mov_b32 m0, s37
	ds_read_b128 v[174:177], v205
	ds_read_b128 v[178:181], v205 offset:1024
	ds_read_b128 v[182:185], v205 offset:2048
	ds_read_b128 v[206:209], v205 offset:3072
	ds_read_b128 v[210:213], v205 offset:4096
	ds_read_b128 v[214:217], v205 offset:5120
	ds_read_b128 v[224:227], v205 offset:6144
	ds_read_b128 v[228:231], v205 offset:7168
	buffer_load_dwordx4 v143, s[56:59], s0 offen lds
	s_mov_b32 m0, s42
	s_nop 0
	buffer_load_dwordx4 v198, s[56:59], s0 offen lds
	s_waitcnt vmcnt(8)
	s_waitcnt lgkmcnt(0)
	s_barrier
	s_waitcnt lgkmcnt(7)
	v_mfma_i32_16x16x64_i8 v[124:127], v[130:133], v[174:177], v[124:127]
	v_mfma_i32_16x16x64_i8 v[120:123], v[138:141], v[174:177], v[120:123]
	s_waitcnt lgkmcnt(5)
	v_mfma_i32_16x16x64_i8 v[116:119], v[130:133], v[182:185], v[116:119]
	v_mfma_i32_16x16x64_i8 v[112:115], v[138:141], v[182:185], v[112:115]
	s_waitcnt lgkmcnt(3)
	v_mfma_i32_16x16x64_i8 v[108:111], v[130:133], v[210:213], v[108:111]
	v_mfma_i32_16x16x64_i8 v[104:107], v[138:141], v[210:213], v[104:107]
	s_waitcnt lgkmcnt(1)
	v_mfma_i32_16x16x64_i8 v[100:103], v[130:133], v[224:227], v[100:103]
	v_mfma_i32_16x16x64_i8 v[96:99], v[138:141], v[224:227], v[96:99]
	v_mfma_i32_16x16x64_i8 v[124:127], v[134:137], v[178:181], v[124:127]
	v_mfma_i32_16x16x64_i8 v[120:123], v[144:147], v[178:181], v[120:123]
	v_mfma_i32_16x16x64_i8 v[116:119], v[134:137], v[206:209], v[116:119]
	v_mfma_i32_16x16x64_i8 v[112:115], v[144:147], v[206:209], v[112:115]
	v_mfma_i32_16x16x64_i8 v[108:111], v[134:137], v[214:217], v[108:111]
	v_mfma_i32_16x16x64_i8 v[104:107], v[144:147], v[214:217], v[104:107]
	s_waitcnt lgkmcnt(0)
	v_mfma_i32_16x16x64_i8 v[100:103], v[134:137], v[228:231], v[100:103]
	v_mfma_i32_16x16x64_i8 v[96:99], v[144:147], v[228:231], v[96:99]
	v_mfma_i32_16x16x64_i8 v[92:95], v[148:151], v[174:177], v[92:95]
	v_mfma_i32_16x16x64_i8 v[88:91], v[156:159], v[174:177], v[88:91]
	v_mfma_i32_16x16x64_i8 v[84:87], v[148:151], v[182:185], v[84:87]
	v_mfma_i32_16x16x64_i8 v[80:83], v[156:159], v[182:185], v[80:83]
	v_mfma_i32_16x16x64_i8 v[76:79], v[148:151], v[210:213], v[76:79]
	v_mfma_i32_16x16x64_i8 v[72:75], v[156:159], v[210:213], v[72:75]
	v_mfma_i32_16x16x64_i8 v[68:71], v[148:151], v[224:227], v[68:71]
	v_mfma_i32_16x16x64_i8 v[64:67], v[156:159], v[224:227], v[64:67]
	v_mfma_i32_16x16x64_i8 v[92:95], v[152:155], v[178:181], v[92:95]
	v_mfma_i32_16x16x64_i8 v[88:91], v[162:165], v[178:181], v[88:91]
	v_mfma_i32_16x16x64_i8 v[84:87], v[152:155], v[206:209], v[84:87]
	v_mfma_i32_16x16x64_i8 v[80:83], v[162:165], v[206:209], v[80:83]
	v_mfma_i32_16x16x64_i8 v[76:79], v[152:155], v[214:217], v[76:79]
	v_mfma_i32_16x16x64_i8 v[72:75], v[162:165], v[214:217], v[72:75]
	v_mfma_i32_16x16x64_i8 v[68:71], v[152:155], v[228:231], v[68:71]
	v_mfma_i32_16x16x64_i8 v[64:67], v[162:165], v[228:231], v[64:67]
	s_barrier
	s_mov_b32 m0, s19
	ds_read_b128 v[174:177], v205 offset:16384
	ds_read_b128 v[178:181], v205 offset:17408
	ds_read_b128 v[182:185], v205 offset:18432
	ds_read_b128 v[206:209], v205 offset:19456
	ds_read_b128 v[210:213], v205 offset:20480
	ds_read_b128 v[214:217], v205 offset:21504
	ds_read_b128 v[224:227], v205 offset:22528
	ds_read_b128 v[228:231], v205 offset:23552
	buffer_load_dwordx4 v161, s[56:59], s33 offen lds
	s_mov_b32 m0, s20
	s_add_i32 s52, s33, 0x40000
	buffer_load_dwordx4 v199, s[56:59], s33 offen lds
	s_mov_b32 m0, s21
	s_nop 0
	buffer_load_dwordx4 v161, s[56:59], s52 offen lds
	s_mov_b32 m0, s22
	s_nop 0
	buffer_load_dwordx4 v199, s[56:59], s52 offen lds
	s_mov_b32 m0, s18
	s_nop 0
	buffer_load_dwordx4 v143, s[56:59], s49 offen lds
	s_mov_b32 m0, s23
	s_nop 0
	buffer_load_dwordx4 v198, s[56:59], s49 offen lds
	s_waitcnt vmcnt(8)
	s_waitcnt lgkmcnt(0)
	s_barrier
	s_waitcnt lgkmcnt(7)
	v_mfma_i32_16x16x64_i8 v[60:63], v[130:133], v[174:177], v[60:63]
	v_mfma_i32_16x16x64_i8 v[56:59], v[138:141], v[174:177], v[56:59]
	s_waitcnt lgkmcnt(5)
	v_mfma_i32_16x16x64_i8 v[52:55], v[130:133], v[182:185], v[52:55]
	v_mfma_i32_16x16x64_i8 v[48:51], v[138:141], v[182:185], v[48:51]
	s_waitcnt lgkmcnt(3)
	v_mfma_i32_16x16x64_i8 v[44:47], v[130:133], v[210:213], v[44:47]
	v_mfma_i32_16x16x64_i8 v[40:43], v[138:141], v[210:213], v[40:43]
	s_waitcnt lgkmcnt(1)
	v_mfma_i32_16x16x64_i8 v[36:39], v[130:133], v[224:227], v[36:39]
	v_mfma_i32_16x16x64_i8 v[32:35], v[138:141], v[224:227], v[32:35]
	v_mfma_i32_16x16x64_i8 v[60:63], v[134:137], v[178:181], v[60:63]
	v_mfma_i32_16x16x64_i8 v[56:59], v[144:147], v[178:181], v[56:59]
	v_mfma_i32_16x16x64_i8 v[52:55], v[134:137], v[206:209], v[52:55]
	v_mfma_i32_16x16x64_i8 v[48:51], v[144:147], v[206:209], v[48:51]
	v_mfma_i32_16x16x64_i8 v[44:47], v[134:137], v[214:217], v[44:47]
	v_mfma_i32_16x16x64_i8 v[40:43], v[144:147], v[214:217], v[40:43]
	s_waitcnt lgkmcnt(0)
	v_mfma_i32_16x16x64_i8 v[36:39], v[134:137], v[228:231], v[36:39]
	v_mfma_i32_16x16x64_i8 v[32:35], v[144:147], v[228:231], v[32:35]
	v_mfma_i32_16x16x64_i8 v[28:31], v[148:151], v[174:177], v[28:31]
	v_mfma_i32_16x16x64_i8 v[24:27], v[156:159], v[174:177], v[24:27]
	v_mfma_i32_16x16x64_i8 v[20:23], v[148:151], v[182:185], v[20:23]
	v_mfma_i32_16x16x64_i8 v[16:19], v[156:159], v[182:185], v[16:19]
	v_mfma_i32_16x16x64_i8 v[12:15], v[148:151], v[210:213], v[12:15]
	v_mfma_i32_16x16x64_i8 v[8:11], v[156:159], v[210:213], v[8:11]
	v_mfma_i32_16x16x64_i8 v[4:7], v[148:151], v[224:227], v[4:7]
	v_mfma_i32_16x16x64_i8 v[0:3], v[156:159], v[224:227], v[0:3]
	v_mfma_i32_16x16x64_i8 v[28:31], v[152:155], v[178:181], v[28:31]
	v_mfma_i32_16x16x64_i8 v[24:27], v[162:165], v[178:181], v[24:27]
	v_mfma_i32_16x16x64_i8 v[20:23], v[152:155], v[206:209], v[20:23]
	v_mfma_i32_16x16x64_i8 v[16:19], v[162:165], v[206:209], v[16:19]
	v_mfma_i32_16x16x64_i8 v[12:15], v[152:155], v[214:217], v[12:15]
	v_mfma_i32_16x16x64_i8 v[8:11], v[162:165], v[214:217], v[8:11]
	v_mfma_i32_16x16x64_i8 v[4:7], v[152:155], v[228:231], v[4:7]
	v_mfma_i32_16x16x64_i8 v[0:3], v[162:165], v[228:231], v[0:3]
	s_barrier
	ds_read_b128 v[130:133], v204 offset:32768
	ds_read_b128 v[134:137], v204 offset:33792
	ds_read_b128 v[138:141], v204 offset:34816
	ds_read_b128 v[144:147], v204 offset:35840
	ds_read_b128 v[148:151], v204 offset:49152
	ds_read_b128 v[152:155], v204 offset:50176
	ds_read_b128 v[156:159], v204 offset:51200
	ds_read_b128 v[162:165], v204 offset:52224
	s_add_i32 s49, s49, 0x40000
	s_mov_b32 m0, s25
	ds_read_b128 v[174:177], v205 offset:32768
	ds_read_b128 v[178:181], v205 offset:33792
	ds_read_b128 v[182:185], v205 offset:34816
	ds_read_b128 v[206:209], v205 offset:35840
	ds_read_b128 v[210:213], v205 offset:36864
	ds_read_b128 v[214:217], v205 offset:37888
	ds_read_b128 v[224:227], v205 offset:38912
	ds_read_b128 v[228:231], v205 offset:39936
	buffer_load_dwordx4 v143, s[56:59], s49 offen lds
	s_mov_b32 m0, s26
	s_nop 0
	buffer_load_dwordx4 v198, s[56:59], s49 offen lds
	s_waitcnt vmcnt(8)
	s_waitcnt lgkmcnt(0)
	s_barrier
	s_waitcnt lgkmcnt(7)
	v_mfma_i32_16x16x64_i8 v[124:127], v[130:133], v[174:177], v[124:127]
	v_mfma_i32_16x16x64_i8 v[120:123], v[138:141], v[174:177], v[120:123]
	s_waitcnt lgkmcnt(5)
	v_mfma_i32_16x16x64_i8 v[116:119], v[130:133], v[182:185], v[116:119]
	v_mfma_i32_16x16x64_i8 v[112:115], v[138:141], v[182:185], v[112:115]
	s_waitcnt lgkmcnt(3)
	v_mfma_i32_16x16x64_i8 v[108:111], v[130:133], v[210:213], v[108:111]
	v_mfma_i32_16x16x64_i8 v[104:107], v[138:141], v[210:213], v[104:107]
	s_waitcnt lgkmcnt(1)
	v_mfma_i32_16x16x64_i8 v[100:103], v[130:133], v[224:227], v[100:103]
	v_mfma_i32_16x16x64_i8 v[96:99], v[138:141], v[224:227], v[96:99]
	v_mfma_i32_16x16x64_i8 v[124:127], v[134:137], v[178:181], v[124:127]
	v_mfma_i32_16x16x64_i8 v[120:123], v[144:147], v[178:181], v[120:123]
	v_mfma_i32_16x16x64_i8 v[116:119], v[134:137], v[206:209], v[116:119]
	v_mfma_i32_16x16x64_i8 v[112:115], v[144:147], v[206:209], v[112:115]
	v_mfma_i32_16x16x64_i8 v[108:111], v[134:137], v[214:217], v[108:111]
	v_mfma_i32_16x16x64_i8 v[104:107], v[144:147], v[214:217], v[104:107]
	s_waitcnt lgkmcnt(0)
	v_mfma_i32_16x16x64_i8 v[100:103], v[134:137], v[228:231], v[100:103]
	v_mfma_i32_16x16x64_i8 v[96:99], v[144:147], v[228:231], v[96:99]
	v_mfma_i32_16x16x64_i8 v[92:95], v[148:151], v[174:177], v[92:95]
	v_mfma_i32_16x16x64_i8 v[88:91], v[156:159], v[174:177], v[88:91]
	v_mfma_i32_16x16x64_i8 v[84:87], v[148:151], v[182:185], v[84:87]
	v_mfma_i32_16x16x64_i8 v[80:83], v[156:159], v[182:185], v[80:83]
	v_mfma_i32_16x16x64_i8 v[76:79], v[148:151], v[210:213], v[76:79]
	v_mfma_i32_16x16x64_i8 v[72:75], v[156:159], v[210:213], v[72:75]
	v_mfma_i32_16x16x64_i8 v[68:71], v[148:151], v[224:227], v[68:71]
	v_mfma_i32_16x16x64_i8 v[64:67], v[156:159], v[224:227], v[64:67]
	v_mfma_i32_16x16x64_i8 v[92:95], v[152:155], v[178:181], v[92:95]
	v_mfma_i32_16x16x64_i8 v[88:91], v[162:165], v[178:181], v[88:91]
	v_mfma_i32_16x16x64_i8 v[84:87], v[152:155], v[206:209], v[84:87]
	v_mfma_i32_16x16x64_i8 v[80:83], v[162:165], v[206:209], v[80:83]
	v_mfma_i32_16x16x64_i8 v[76:79], v[152:155], v[214:217], v[76:79]
	v_mfma_i32_16x16x64_i8 v[72:75], v[162:165], v[214:217], v[72:75]
	v_mfma_i32_16x16x64_i8 v[68:71], v[152:155], v[228:231], v[68:71]
	v_mfma_i32_16x16x64_i8 v[64:67], v[162:165], v[228:231], v[64:67]
	s_barrier
	s_mov_b32 m0, s27
	s_add_i32 s49, s33, 0x80
	ds_read_b128 v[174:177], v205 offset:49152
	ds_read_b128 v[178:181], v205 offset:50176
	ds_read_b128 v[182:185], v205 offset:51200
	ds_read_b128 v[206:209], v205 offset:52224
	ds_read_b128 v[210:213], v205 offset:53248
	ds_read_b128 v[214:217], v205 offset:54272
	ds_read_b128 v[224:227], v205 offset:55296
	ds_read_b128 v[228:231], v205 offset:56320
	buffer_load_dwordx4 v161, s[56:59], s49 offen lds
	s_mov_b32 m0, s28
	s_add_i32 s33, s33, 0x40080
	buffer_load_dwordx4 v199, s[56:59], s49 offen lds
	s_mov_b32 m0, s31
	s_nop 0
	buffer_load_dwordx4 v161, s[56:59], s33 offen lds
	s_mov_b32 m0, s36
	s_nop 0
	buffer_load_dwordx4 v199, s[56:59], s33 offen lds
	s_mov_b32 m0, s29
	s_nop 0
	buffer_load_dwordx4 v143, s[56:59], s15 offen lds
	s_mov_b32 m0, s30
	s_nop 0
	buffer_load_dwordx4 v198, s[56:59], s15 offen lds
	s_waitcnt vmcnt(8)
	s_waitcnt lgkmcnt(0)
	s_barrier
	s_waitcnt lgkmcnt(7)
	v_mfma_i32_16x16x64_i8 v[60:63], v[130:133], v[174:177], v[60:63]
	v_mfma_i32_16x16x64_i8 v[56:59], v[138:141], v[174:177], v[56:59]
	s_waitcnt lgkmcnt(5)
	v_mfma_i32_16x16x64_i8 v[52:55], v[130:133], v[182:185], v[52:55]
	v_mfma_i32_16x16x64_i8 v[48:51], v[138:141], v[182:185], v[48:51]
	s_waitcnt lgkmcnt(3)
	v_mfma_i32_16x16x64_i8 v[44:47], v[130:133], v[210:213], v[44:47]
	v_mfma_i32_16x16x64_i8 v[40:43], v[138:141], v[210:213], v[40:43]
	s_waitcnt lgkmcnt(1)
	v_mfma_i32_16x16x64_i8 v[36:39], v[130:133], v[224:227], v[36:39]
	v_mfma_i32_16x16x64_i8 v[32:35], v[138:141], v[224:227], v[32:35]
	v_mfma_i32_16x16x64_i8 v[60:63], v[134:137], v[178:181], v[60:63]
	v_mfma_i32_16x16x64_i8 v[56:59], v[144:147], v[178:181], v[56:59]
	v_mfma_i32_16x16x64_i8 v[52:55], v[134:137], v[206:209], v[52:55]
	v_mfma_i32_16x16x64_i8 v[48:51], v[144:147], v[206:209], v[48:51]
	v_mfma_i32_16x16x64_i8 v[44:47], v[134:137], v[214:217], v[44:47]
	v_mfma_i32_16x16x64_i8 v[40:43], v[144:147], v[214:217], v[40:43]
	s_waitcnt lgkmcnt(0)
	v_mfma_i32_16x16x64_i8 v[36:39], v[134:137], v[228:231], v[36:39]
	v_mfma_i32_16x16x64_i8 v[32:35], v[144:147], v[228:231], v[32:35]
	v_mfma_i32_16x16x64_i8 v[28:31], v[148:151], v[174:177], v[28:31]
	v_mfma_i32_16x16x64_i8 v[24:27], v[156:159], v[174:177], v[24:27]
	v_mfma_i32_16x16x64_i8 v[20:23], v[148:151], v[182:185], v[20:23]
	v_mfma_i32_16x16x64_i8 v[16:19], v[156:159], v[182:185], v[16:19]
	v_mfma_i32_16x16x64_i8 v[12:15], v[148:151], v[210:213], v[12:15]
	v_mfma_i32_16x16x64_i8 v[8:11], v[156:159], v[210:213], v[8:11]
	v_mfma_i32_16x16x64_i8 v[4:7], v[148:151], v[224:227], v[4:7]
	v_mfma_i32_16x16x64_i8 v[0:3], v[156:159], v[224:227], v[0:3]
	v_mfma_i32_16x16x64_i8 v[28:31], v[152:155], v[178:181], v[28:31]
	v_mfma_i32_16x16x64_i8 v[24:27], v[162:165], v[178:181], v[24:27]
	v_mfma_i32_16x16x64_i8 v[20:23], v[152:155], v[206:209], v[20:23]
	v_mfma_i32_16x16x64_i8 v[16:19], v[162:165], v[206:209], v[16:19]
	v_mfma_i32_16x16x64_i8 v[12:15], v[152:155], v[214:217], v[12:15]
	v_mfma_i32_16x16x64_i8 v[8:11], v[162:165], v[214:217], v[8:11]
	v_mfma_i32_16x16x64_i8 v[4:7], v[152:155], v[228:231], v[4:7]
	v_mfma_i32_16x16x64_i8 v[0:3], v[162:165], v[228:231], v[0:3]
	s_barrier
	s_add_i32 s14, s14, 2
	s_addk_i32 s0, 0x100
	s_addk_i32 s1, 0x100
	s_cmp_gt_u32 s14, 13
	s_cbranch_scc0 .LBB0_965
	s_and_b64 vcc, exec, s[16:17]
	s_cbranch_vccz .LBB0_968
	s_barrier

.LBB0_983:
	ds_read_b128 v[16:19], v205
	ds_read_b128 v[20:23], v205 offset:1024
	ds_read_b128 v[24:27], v205 offset:2048
	ds_read_b128 v[28:31], v205 offset:3072
	ds_read_b128 v[0:3], v205 offset:16384
	ds_read_b128 v[4:7], v205 offset:17408
	ds_read_b128 v[8:11], v205 offset:18432
	ds_read_b128 v[12:15], v205 offset:19456
	s_add_i32 s14, s0, 0xfffc0080
	s_cmp_eq_u32 s13, 12
	s_cselect_b32 s33, s47, s14
	s_cselect_b32 s15, s48, s1
	s_add_i32 s14, s33, 0x80
	s_mov_b32 s56, s78
	s_mov_b32 m0, s41
	ds_read_b128 v[174:177], v206
	ds_read_b128 v[178:181], v206 offset:1024
	ds_read_b128 v[208:211], v206 offset:2048
	ds_read_b128 v[212:215], v206 offset:3072
	ds_read_b128 v[224:227], v206 offset:4096
	ds_read_b128 v[228:231], v206 offset:5120
	ds_read_b128 v[232:235], v206 offset:6144
	ds_read_b128 v[236:239], v206 offset:7168
	buffer_load_dwordx4 v182, s[56:59], s0 offen lds
	s_mov_b32 m0, s42
	s_nop 0
	buffer_load_dwordx4 v184, s[56:59], s0 offen lds
	s_waitcnt vmcnt(8)
	s_waitcnt lgkmcnt(0)
	s_barrier
	s_waitcnt lgkmcnt(6)
	v_mfma_f32_16x16x128_f8f6f4 v[156:159], v[16:23], v[174:181], v[156:159]
	v_mfma_f32_16x16x128_f8f6f4 v[148:151], v[24:31], v[174:181], v[148:151]
	s_waitcnt lgkmcnt(4)
	v_mfma_f32_16x16x128_f8f6f4 v[140:143], v[16:23], v[208:215], v[140:143]
	v_mfma_f32_16x16x128_f8f6f4 v[132:135], v[24:31], v[208:215], v[132:135]
	s_waitcnt lgkmcnt(2)
	v_mfma_f32_16x16x128_f8f6f4 v[124:127], v[16:23], v[224:231], v[124:127]
	v_mfma_f32_16x16x128_f8f6f4 v[116:119], v[24:31], v[224:231], v[116:119]
	s_waitcnt lgkmcnt(0)
	v_mfma_f32_16x16x128_f8f6f4 v[108:111], v[16:23], v[232:239], v[108:111]
	v_mfma_f32_16x16x128_f8f6f4 v[100:103], v[24:31], v[232:239], v[100:103]
	v_mfma_f32_16x16x128_f8f6f4 v[152:155], v[0:7], v[174:181], v[152:155]
	v_mfma_f32_16x16x128_f8f6f4 v[144:147], v[8:15], v[174:181], v[144:147]
	v_mfma_f32_16x16x128_f8f6f4 v[136:139], v[0:7], v[208:215], v[136:139]
	v_mfma_f32_16x16x128_f8f6f4 v[128:131], v[8:15], v[208:215], v[128:131]
	v_mfma_f32_16x16x128_f8f6f4 v[120:123], v[0:7], v[224:231], v[120:123]
	v_mfma_f32_16x16x128_f8f6f4 v[112:115], v[8:15], v[224:231], v[112:115]
	v_mfma_f32_16x16x128_f8f6f4 v[104:107], v[0:7], v[232:239], v[104:107]
	v_mfma_f32_16x16x128_f8f6f4 v[96:99], v[8:15], v[232:239], v[96:99]
	s_barrier
	s_mov_b32 m0, s9
	ds_read_b128 v[174:177], v206 offset:16384
	ds_read_b128 v[178:181], v206 offset:17408
	ds_read_b128 v[208:211], v206 offset:18432
	ds_read_b128 v[212:215], v206 offset:19456
	ds_read_b128 v[224:227], v206 offset:20480
	ds_read_b128 v[228:231], v206 offset:21504
	ds_read_b128 v[232:235], v206 offset:22528
	ds_read_b128 v[236:239], v206 offset:23552
	buffer_load_dwordx4 v183, s[56:59], s15 offen lds
	s_mov_b32 m0, s10
	s_add_i32 s49, s15, 0x40000
	buffer_load_dwordx4 v185, s[56:59], s15 offen lds
	s_mov_b32 m0, s11
	s_nop 0
	buffer_load_dwordx4 v183, s[56:59], s49 offen lds
	s_mov_b32 m0, s25
	s_nop 0
	buffer_load_dwordx4 v185, s[56:59], s49 offen lds
	s_mov_b32 m0, s8
	s_nop 0
	buffer_load_dwordx4 v182, s[56:59], s33 offen lds
	s_mov_b32 m0, s26
	s_nop 0
	buffer_load_dwordx4 v184, s[56:59], s33 offen lds
	s_waitcnt vmcnt(8)
	s_waitcnt lgkmcnt(0)
	s_barrier
	s_waitcnt lgkmcnt(6)
	v_mfma_f32_16x16x128_f8f6f4 v[92:95], v[16:23], v[174:181], v[92:95]
	v_mfma_f32_16x16x128_f8f6f4 v[84:87], v[24:31], v[174:181], v[84:87]
	s_waitcnt lgkmcnt(4)
	v_mfma_f32_16x16x128_f8f6f4 v[76:79], v[16:23], v[208:215], v[76:79]
	v_mfma_f32_16x16x128_f8f6f4 v[68:71], v[24:31], v[208:215], v[68:71]
	s_waitcnt lgkmcnt(2)
	v_mfma_f32_16x16x128_f8f6f4 v[60:63], v[16:23], v[224:231], v[60:63]
	v_mfma_f32_16x16x128_f8f6f4 v[52:55], v[24:31], v[224:231], v[52:55]
	s_waitcnt lgkmcnt(0)
	v_mfma_f32_16x16x128_f8f6f4 v[44:47], v[16:23], v[232:239], v[44:47]
	v_mfma_f32_16x16x128_f8f6f4 v[36:39], v[24:31], v[232:239], v[36:39]
	v_mfma_f32_16x16x128_f8f6f4 v[88:91], v[0:7], v[174:181], v[88:91]
	v_mfma_f32_16x16x128_f8f6f4 v[80:83], v[8:15], v[174:181], v[80:83]
	v_mfma_f32_16x16x128_f8f6f4 v[72:75], v[0:7], v[208:215], v[72:75]
	v_mfma_f32_16x16x128_f8f6f4 v[64:67], v[8:15], v[208:215], v[64:67]
	v_mfma_f32_16x16x128_f8f6f4 v[56:59], v[0:7], v[224:231], v[56:59]
	v_mfma_f32_16x16x128_f8f6f4 v[48:51], v[8:15], v[224:231], v[48:51]
	v_mfma_f32_16x16x128_f8f6f4 v[40:43], v[0:7], v[232:239], v[40:43]
	v_mfma_f32_16x16x128_f8f6f4 v[32:35], v[8:15], v[232:239], v[32:35]
	s_barrier
	ds_read_b128 v[0:3], v205 offset:32768
	ds_read_b128 v[4:7], v205 offset:33792
	ds_read_b128 v[8:11], v205 offset:34816
	ds_read_b128 v[12:15], v205 offset:35840
	ds_read_b128 v[16:19], v205 offset:49152
	ds_read_b128 v[20:23], v205 offset:50176
	ds_read_b128 v[24:27], v205 offset:51200
	ds_read_b128 v[28:31], v205 offset:52224
	s_add_i32 s33, s33, 0x40000
	s_mov_b32 m0, s27
	ds_read_b128 v[174:177], v206 offset:32768
	ds_read_b128 v[178:181], v206 offset:33792
	ds_read_b128 v[208:211], v206 offset:34816
	ds_read_b128 v[212:215], v206 offset:35840
	ds_read_b128 v[224:227], v206 offset:36864
	ds_read_b128 v[228:231], v206 offset:37888
	ds_read_b128 v[232:235], v206 offset:38912
	ds_read_b128 v[236:239], v206 offset:39936
	buffer_load_dwordx4 v182, s[56:59], s33 offen lds
	s_mov_b32 m0, s28
	s_nop 0
	buffer_load_dwordx4 v184, s[56:59], s33 offen lds
	s_waitcnt vmcnt(8)
	s_waitcnt lgkmcnt(0)
	s_barrier
	s_waitcnt lgkmcnt(6)
	v_mfma_f32_16x16x128_f8f6f4 v[156:159], v[0:7], v[174:181], v[156:159]
	v_mfma_f32_16x16x128_f8f6f4 v[148:151], v[8:15], v[174:181], v[148:151]
	s_waitcnt lgkmcnt(4)
	v_mfma_f32_16x16x128_f8f6f4 v[140:143], v[0:7], v[208:215], v[140:143]
	v_mfma_f32_16x16x128_f8f6f4 v[132:135], v[8:15], v[208:215], v[132:135]
	s_waitcnt lgkmcnt(2)
	v_mfma_f32_16x16x128_f8f6f4 v[124:127], v[0:7], v[224:231], v[124:127]
	v_mfma_f32_16x16x128_f8f6f4 v[116:119], v[8:15], v[224:231], v[116:119]
	s_waitcnt lgkmcnt(0)
	v_mfma_f32_16x16x128_f8f6f4 v[108:111], v[0:7], v[232:239], v[108:111]
	v_mfma_f32_16x16x128_f8f6f4 v[100:103], v[8:15], v[232:239], v[100:103]
	v_mfma_f32_16x16x128_f8f6f4 v[152:155], v[16:23], v[174:181], v[152:155]
	v_mfma_f32_16x16x128_f8f6f4 v[144:147], v[24:31], v[174:181], v[144:147]
	v_mfma_f32_16x16x128_f8f6f4 v[136:139], v[16:23], v[208:215], v[136:139]
	v_mfma_f32_16x16x128_f8f6f4 v[128:131], v[24:31], v[208:215], v[128:131]
	v_mfma_f32_16x16x128_f8f6f4 v[120:123], v[16:23], v[224:231], v[120:123]
	v_mfma_f32_16x16x128_f8f6f4 v[112:115], v[24:31], v[224:231], v[112:115]
	v_mfma_f32_16x16x128_f8f6f4 v[104:107], v[16:23], v[232:239], v[104:107]
	v_mfma_f32_16x16x128_f8f6f4 v[96:99], v[24:31], v[232:239], v[96:99]
	s_barrier
	s_mov_b32 m0, s29
	s_add_i32 s33, s15, 0x80
	ds_read_b128 v[174:177], v206 offset:49152
	ds_read_b128 v[178:181], v206 offset:50176
	ds_read_b128 v[208:211], v206 offset:51200
	ds_read_b128 v[212:215], v206 offset:52224
	ds_read_b128 v[224:227], v206 offset:53248
	ds_read_b128 v[228:231], v206 offset:54272
	ds_read_b128 v[232:235], v206 offset:55296
	ds_read_b128 v[236:239], v206 offset:56320
	buffer_load_dwordx4 v183, s[56:59], s33 offen lds
	s_mov_b32 m0, s30
	s_add_i32 s15, s15, 0x40080
	buffer_load_dwordx4 v185, s[56:59], s33 offen lds
	s_mov_b32 m0, s37
	s_nop 0
	buffer_load_dwordx4 v183, s[56:59], s15 offen lds
	s_mov_b32 m0, s40
	s_nop 0
	buffer_load_dwordx4 v185, s[56:59], s15 offen lds
	s_mov_b32 m0, s31
	s_nop 0
	buffer_load_dwordx4 v182, s[56:59], s14 offen lds
	s_mov_b32 m0, s36
	s_nop 0
	buffer_load_dwordx4 v184, s[56:59], s14 offen lds
	s_waitcnt vmcnt(8)
	s_waitcnt lgkmcnt(0)
	s_barrier
	s_waitcnt lgkmcnt(6)
	v_mfma_f32_16x16x128_f8f6f4 v[92:95], v[0:7], v[174:181], v[92:95]
	v_mfma_f32_16x16x128_f8f6f4 v[84:87], v[8:15], v[174:181], v[84:87]
	s_waitcnt lgkmcnt(4)
	v_mfma_f32_16x16x128_f8f6f4 v[76:79], v[0:7], v[208:215], v[76:79]
	v_mfma_f32_16x16x128_f8f6f4 v[68:71], v[8:15], v[208:215], v[68:71]
	s_waitcnt lgkmcnt(2)
	v_mfma_f32_16x16x128_f8f6f4 v[60:63], v[0:7], v[224:231], v[60:63]
	v_mfma_f32_16x16x128_f8f6f4 v[52:55], v[8:15], v[224:231], v[52:55]
	s_waitcnt lgkmcnt(0)
	v_mfma_f32_16x16x128_f8f6f4 v[44:47], v[0:7], v[232:239], v[44:47]
	v_mfma_f32_16x16x128_f8f6f4 v[36:39], v[8:15], v[232:239], v[36:39]
	v_mfma_f32_16x16x128_f8f6f4 v[88:91], v[16:23], v[174:181], v[88:91]
	v_mfma_f32_16x16x128_f8f6f4 v[80:83], v[24:31], v[174:181], v[80:83]
	v_mfma_f32_16x16x128_f8f6f4 v[72:75], v[16:23], v[208:215], v[72:75]
	v_mfma_f32_16x16x128_f8f6f4 v[64:67], v[24:31], v[208:215], v[64:67]
	v_mfma_f32_16x16x128_f8f6f4 v[56:59], v[16:23], v[224:231], v[56:59]
	v_mfma_f32_16x16x128_f8f6f4 v[48:51], v[24:31], v[224:231], v[48:51]
	v_mfma_f32_16x16x128_f8f6f4 v[40:43], v[16:23], v[232:239], v[40:43]
	v_mfma_f32_16x16x128_f8f6f4 v[32:35], v[24:31], v[232:239], v[32:35]
	s_barrier
	s_add_i32 s13, s13, 2
	s_addk_i32 s0, 0x100
	s_addk_i32 s1, 0x100
	s_cmp_gt_u32 s13, 13
	s_cbranch_scc0 .LBB0_983
	s_and_b64 vcc, exec, s[22:23]
	s_cbranch_vccz .LBB0_986
	s_barrier

.LBB0_1158:
	ds_read_b128 v[16:19], v182
	ds_read_b128 v[20:23], v182 offset:1024
	ds_read_b128 v[24:27], v182 offset:2048
	ds_read_b128 v[28:31], v182 offset:3072
	s_waitcnt lgkmcnt(4)
	ds_read_b128 v[0:3], v182 offset:16384
	ds_read_b128 v[4:7], v182 offset:17408
	ds_read_b128 v[8:11], v182 offset:18432
	ds_read_b128 v[12:15], v182 offset:19456
	s_add_i32 s13, s8, 0xfff50080
	s_cmp_eq_u32 s12, 40
	s_cselect_b32 s15, s42, s13
	s_cselect_b32 s14, s43, s9
	s_add_i32 s13, s15, 0x80
	s_mov_b32 s56, s78
	s_mov_b32 m0, s31
	ds_read_b128 v[174:177], v183
	ds_read_b128 v[178:181], v183 offset:1024
	ds_read_b128 v[198:201], v183 offset:2048
	ds_read_b128 v[202:205], v183 offset:3072
	ds_read_b128 v[206:209], v183 offset:4096
	ds_read_b128 v[210:213], v183 offset:5120
	ds_read_b128 v[224:227], v183 offset:6144
	ds_read_b128 v[228:231], v183 offset:7168
	buffer_load_dwordx4 v160, s[56:59], s8 offen lds
	s_mov_b32 m0, s35
	s_nop 0
	buffer_load_dwordx4 v162, s[56:59], s8 offen lds
	s_waitcnt vmcnt(8)
	s_waitcnt lgkmcnt(0)
	s_barrier
	s_waitcnt lgkmcnt(6)
	v_mfma_f32_16x16x128_f8f6f4 v[156:159], v[16:23], v[174:181], v[156:159]
	v_mfma_f32_16x16x128_f8f6f4 v[152:155], v[24:31], v[174:181], v[152:155]
	s_waitcnt lgkmcnt(4)
	v_mfma_f32_16x16x128_f8f6f4 v[140:143], v[16:23], v[198:205], v[140:143]
	v_mfma_f32_16x16x128_f8f6f4 v[136:139], v[24:31], v[198:205], v[136:139]
	s_waitcnt lgkmcnt(2)
	v_mfma_f32_16x16x128_f8f6f4 v[124:127], v[16:23], v[206:213], v[124:127]
	v_mfma_f32_16x16x128_f8f6f4 v[120:123], v[24:31], v[206:213], v[120:123]
	s_waitcnt lgkmcnt(0)
	v_mfma_f32_16x16x128_f8f6f4 v[108:111], v[16:23], v[224:231], v[108:111]
	v_mfma_f32_16x16x128_f8f6f4 v[104:107], v[24:31], v[224:231], v[104:107]
	v_mfma_f32_16x16x128_f8f6f4 v[148:151], v[0:7], v[174:181], v[148:151]
	v_mfma_f32_16x16x128_f8f6f4 v[144:147], v[8:15], v[174:181], v[144:147]
	v_mfma_f32_16x16x128_f8f6f4 v[132:135], v[0:7], v[198:205], v[132:135]
	v_mfma_f32_16x16x128_f8f6f4 v[128:131], v[8:15], v[198:205], v[128:131]
	v_mfma_f32_16x16x128_f8f6f4 v[116:119], v[0:7], v[206:213], v[116:119]
	v_mfma_f32_16x16x128_f8f6f4 v[112:115], v[8:15], v[206:213], v[112:115]
	v_mfma_f32_16x16x128_f8f6f4 v[100:103], v[0:7], v[224:231], v[100:103]
	v_mfma_f32_16x16x128_f8f6f4 v[96:99], v[8:15], v[224:231], v[96:99]
	s_barrier
	s_mov_b32 m0, s18
	ds_read_b128 v[174:177], v183 offset:16384
	ds_read_b128 v[178:181], v183 offset:17408
	ds_read_b128 v[198:201], v183 offset:18432
	ds_read_b128 v[202:205], v183 offset:19456
	ds_read_b128 v[206:209], v183 offset:20480
	ds_read_b128 v[210:213], v183 offset:21504
	ds_read_b128 v[224:227], v183 offset:22528
	ds_read_b128 v[228:231], v183 offset:23552
	buffer_load_dwordx4 v161, s[56:59], s14 offen lds
	s_mov_b32 m0, s19
	s_add_i32 s33, s14, 0xb0000
	buffer_load_dwordx4 v163, s[56:59], s14 offen lds
	s_mov_b32 m0, s20
	s_nop 0
	buffer_load_dwordx4 v161, s[56:59], s33 offen lds
	s_mov_b32 m0, s21
	s_nop 0
	buffer_load_dwordx4 v163, s[56:59], s33 offen lds
	s_mov_b32 m0, s7
	s_nop 0
	buffer_load_dwordx4 v160, s[56:59], s15 offen lds
	s_mov_b32 m0, s22
	s_nop 0
	buffer_load_dwordx4 v162, s[56:59], s15 offen lds
	s_waitcnt vmcnt(8)
	s_waitcnt lgkmcnt(0)
	s_barrier
	s_waitcnt lgkmcnt(6)
	v_mfma_f32_16x16x128_f8f6f4 v[92:95], v[16:23], v[174:181], v[92:95]
	v_mfma_f32_16x16x128_f8f6f4 v[88:91], v[24:31], v[174:181], v[88:91]
	s_waitcnt lgkmcnt(4)
	v_mfma_f32_16x16x128_f8f6f4 v[76:79], v[16:23], v[198:205], v[76:79]
	v_mfma_f32_16x16x128_f8f6f4 v[72:75], v[24:31], v[198:205], v[72:75]
	s_waitcnt lgkmcnt(2)
	v_mfma_f32_16x16x128_f8f6f4 v[60:63], v[16:23], v[206:213], v[60:63]
	v_mfma_f32_16x16x128_f8f6f4 v[56:59], v[24:31], v[206:213], v[56:59]
	s_waitcnt lgkmcnt(0)
	v_mfma_f32_16x16x128_f8f6f4 v[44:47], v[16:23], v[224:231], v[44:47]
	v_mfma_f32_16x16x128_f8f6f4 v[40:43], v[24:31], v[224:231], v[40:43]
	v_mfma_f32_16x16x128_f8f6f4 v[84:87], v[0:7], v[174:181], v[84:87]
	v_mfma_f32_16x16x128_f8f6f4 v[80:83], v[8:15], v[174:181], v[80:83]
	v_mfma_f32_16x16x128_f8f6f4 v[68:71], v[0:7], v[198:205], v[68:71]
	v_mfma_f32_16x16x128_f8f6f4 v[64:67], v[8:15], v[198:205], v[64:67]
	v_mfma_f32_16x16x128_f8f6f4 v[52:55], v[0:7], v[206:213], v[52:55]
	v_mfma_f32_16x16x128_f8f6f4 v[48:51], v[8:15], v[206:213], v[48:51]
	v_mfma_f32_16x16x128_f8f6f4 v[36:39], v[0:7], v[224:231], v[36:39]
	v_mfma_f32_16x16x128_f8f6f4 v[32:35], v[8:15], v[224:231], v[32:35]
	s_barrier
	ds_read_b128 v[0:3], v182 offset:32768
	ds_read_b128 v[4:7], v182 offset:33792
	ds_read_b128 v[8:11], v182 offset:34816
	ds_read_b128 v[12:15], v182 offset:35840
	ds_read_b128 v[16:19], v182 offset:49152
	ds_read_b128 v[20:23], v182 offset:50176
	ds_read_b128 v[24:27], v182 offset:51200
	ds_read_b128 v[28:31], v182 offset:52224
	s_add_i32 s15, s15, 0xb0000
	s_mov_b32 m0, s23
	ds_read_b128 v[174:177], v183 offset:32768
	ds_read_b128 v[178:181], v183 offset:33792
	ds_read_b128 v[198:201], v183 offset:34816
	ds_read_b128 v[202:205], v183 offset:35840
	ds_read_b128 v[206:209], v183 offset:36864
	ds_read_b128 v[210:213], v183 offset:37888
	ds_read_b128 v[224:227], v183 offset:38912
	ds_read_b128 v[228:231], v183 offset:39936
	buffer_load_dwordx4 v160, s[56:59], s15 offen lds
	s_mov_b32 m0, s24
	s_nop 0
	buffer_load_dwordx4 v162, s[56:59], s15 offen lds
	s_waitcnt vmcnt(8)
	s_waitcnt lgkmcnt(0)
	s_barrier
	s_waitcnt lgkmcnt(6)
	v_mfma_f32_16x16x128_f8f6f4 v[156:159], v[0:7], v[174:181], v[156:159]
	v_mfma_f32_16x16x128_f8f6f4 v[152:155], v[8:15], v[174:181], v[152:155]
	s_waitcnt lgkmcnt(4)
	v_mfma_f32_16x16x128_f8f6f4 v[140:143], v[0:7], v[198:205], v[140:143]
	v_mfma_f32_16x16x128_f8f6f4 v[136:139], v[8:15], v[198:205], v[136:139]
	s_waitcnt lgkmcnt(2)
	v_mfma_f32_16x16x128_f8f6f4 v[124:127], v[0:7], v[206:213], v[124:127]
	v_mfma_f32_16x16x128_f8f6f4 v[120:123], v[8:15], v[206:213], v[120:123]
	s_waitcnt lgkmcnt(0)
	v_mfma_f32_16x16x128_f8f6f4 v[108:111], v[0:7], v[224:231], v[108:111]
	v_mfma_f32_16x16x128_f8f6f4 v[104:107], v[8:15], v[224:231], v[104:107]
	v_mfma_f32_16x16x128_f8f6f4 v[148:151], v[16:23], v[174:181], v[148:151]
	v_mfma_f32_16x16x128_f8f6f4 v[144:147], v[24:31], v[174:181], v[144:147]
	v_mfma_f32_16x16x128_f8f6f4 v[132:135], v[16:23], v[198:205], v[132:135]
	v_mfma_f32_16x16x128_f8f6f4 v[128:131], v[24:31], v[198:205], v[128:131]
	v_mfma_f32_16x16x128_f8f6f4 v[116:119], v[16:23], v[206:213], v[116:119]
	v_mfma_f32_16x16x128_f8f6f4 v[112:115], v[24:31], v[206:213], v[112:115]
	v_mfma_f32_16x16x128_f8f6f4 v[100:103], v[16:23], v[224:231], v[100:103]
	v_mfma_f32_16x16x128_f8f6f4 v[96:99], v[24:31], v[224:231], v[96:99]
	s_barrier
	s_mov_b32 m0, s25
	s_add_i32 s15, s14, 0x80
	ds_read_b128 v[174:177], v183 offset:49152
	ds_read_b128 v[178:181], v183 offset:50176
	ds_read_b128 v[198:201], v183 offset:51200
	ds_read_b128 v[202:205], v183 offset:52224
	ds_read_b128 v[206:209], v183 offset:53248
	ds_read_b128 v[210:213], v183 offset:54272
	ds_read_b128 v[224:227], v183 offset:55296
	ds_read_b128 v[228:231], v183 offset:56320
	buffer_load_dwordx4 v161, s[56:59], s15 offen lds
	s_mov_b32 m0, s26
	s_add_i32 s14, s14, 0xb0080
	buffer_load_dwordx4 v163, s[56:59], s15 offen lds
	s_mov_b32 m0, s29
	s_nop 0
	buffer_load_dwordx4 v161, s[56:59], s14 offen lds
	s_mov_b32 m0, s30
	s_nop 0
	buffer_load_dwordx4 v163, s[56:59], s14 offen lds
	s_mov_b32 m0, s27
	s_nop 0
	buffer_load_dwordx4 v160, s[56:59], s13 offen lds
	s_mov_b32 m0, s28
	s_nop 0
	buffer_load_dwordx4 v162, s[56:59], s13 offen lds
	s_waitcnt vmcnt(8)
	s_waitcnt lgkmcnt(0)
	s_barrier
	s_waitcnt lgkmcnt(6)
	v_mfma_f32_16x16x128_f8f6f4 v[92:95], v[0:7], v[174:181], v[92:95]
	v_mfma_f32_16x16x128_f8f6f4 v[88:91], v[8:15], v[174:181], v[88:91]
	s_waitcnt lgkmcnt(4)
	v_mfma_f32_16x16x128_f8f6f4 v[76:79], v[0:7], v[198:205], v[76:79]
	v_mfma_f32_16x16x128_f8f6f4 v[72:75], v[8:15], v[198:205], v[72:75]
	s_waitcnt lgkmcnt(2)
	v_mfma_f32_16x16x128_f8f6f4 v[60:63], v[0:7], v[206:213], v[60:63]
	v_mfma_f32_16x16x128_f8f6f4 v[56:59], v[8:15], v[206:213], v[56:59]
	s_waitcnt lgkmcnt(0)
	v_mfma_f32_16x16x128_f8f6f4 v[44:47], v[0:7], v[224:231], v[44:47]
	v_mfma_f32_16x16x128_f8f6f4 v[40:43], v[8:15], v[224:231], v[40:43]
	v_mfma_f32_16x16x128_f8f6f4 v[84:87], v[16:23], v[174:181], v[84:87]
	v_mfma_f32_16x16x128_f8f6f4 v[80:83], v[24:31], v[174:181], v[80:83]
	v_mfma_f32_16x16x128_f8f6f4 v[68:71], v[16:23], v[198:205], v[68:71]
	v_mfma_f32_16x16x128_f8f6f4 v[64:67], v[24:31], v[198:205], v[64:67]
	v_mfma_f32_16x16x128_f8f6f4 v[52:55], v[16:23], v[206:213], v[52:55]
	v_mfma_f32_16x16x128_f8f6f4 v[48:51], v[24:31], v[206:213], v[48:51]
	v_mfma_f32_16x16x128_f8f6f4 v[36:39], v[16:23], v[224:231], v[36:39]
	v_mfma_f32_16x16x128_f8f6f4 v[32:35], v[24:31], v[224:231], v[32:35]
	s_barrier
	s_add_i32 s12, s12, 2
	s_addk_i32 s8, 0x100
	s_addk_i32 s9, 0x100
	s_cmp_gt_u32 s12, 41
	s_cbranch_scc0 .LBB0_1158
	s_and_b64 vcc, exec, s[2:3]
	s_cbranch_vccz .LBB0_1161
	s_barrier

.LBB0_1238:
	ds_read_b128 v[142:145], v140
	ds_read_b128 v[146:149], v140 offset:1024
	ds_read_b128 v[150:153], v140 offset:2048
	ds_read_b128 v[154:157], v140 offset:3072
	ds_read_b128 v[158:161], v140 offset:16384
	ds_read_b128 v[162:165], v140 offset:17408
	ds_read_b128 v[174:177], v140 offset:18432
	ds_read_b128 v[178:181], v140 offset:19456
	s_add_i32 s40, s10, 0xfff80080
	s_cmp_eq_u32 s37, 4
	s_cselect_b32 s42, s35, s40
	s_cselect_b32 s41, s36, s11
	s_add_i32 s40, s42, 0x80
	s_mov_b32 s56, s78
	s_mov_b32 m0, s28
	ds_read_b128 v[182:185], v141
	ds_read_b128 v[198:201], v141 offset:1024
	ds_read_b128 v[202:205], v141 offset:2048
	ds_read_b128 v[206:209], v141 offset:3072
	ds_read_b128 v[210:213], v141 offset:4096
	ds_read_b128 v[214:217], v141 offset:5120
	ds_read_b128 v[224:227], v141 offset:6144
	ds_read_b128 v[228:231], v141 offset:7168
	buffer_load_dwordx4 v128, s[56:59], s10 offen lds
	s_mov_b32 m0, s29
	s_nop 0
	buffer_load_dwordx4 v130, s[56:59], s10 offen lds
	s_waitcnt vmcnt(8)
	s_waitcnt lgkmcnt(0)
	s_barrier
	s_waitcnt lgkmcnt(7)
	v_mfma_f32_16x16x32_bf16 v[124:127], v[142:145], v[182:185], v[124:127]
	v_mfma_f32_16x16x32_bf16 v[120:123], v[150:153], v[182:185], v[120:123]
	s_waitcnt lgkmcnt(5)
	v_mfma_f32_16x16x32_bf16 v[116:119], v[142:145], v[202:205], v[116:119]
	v_mfma_f32_16x16x32_bf16 v[108:111], v[150:153], v[202:205], v[108:111]
	s_waitcnt lgkmcnt(3)
	v_mfma_f32_16x16x32_bf16 v[100:103], v[142:145], v[210:213], v[100:103]
	v_mfma_f32_16x16x32_bf16 v[92:95], v[150:153], v[210:213], v[92:95]
	s_waitcnt lgkmcnt(1)
	v_mfma_f32_16x16x32_bf16 v[84:87], v[142:145], v[224:227], v[84:87]
	v_mfma_f32_16x16x32_bf16 v[76:79], v[150:153], v[224:227], v[76:79]
	v_mfma_f32_16x16x32_bf16 v[124:127], v[146:149], v[198:201], v[124:127]
	v_mfma_f32_16x16x32_bf16 v[120:123], v[154:157], v[198:201], v[120:123]
	v_mfma_f32_16x16x32_bf16 v[116:119], v[146:149], v[206:209], v[116:119]
	v_mfma_f32_16x16x32_bf16 v[108:111], v[154:157], v[206:209], v[108:111]
	v_mfma_f32_16x16x32_bf16 v[100:103], v[146:149], v[214:217], v[100:103]
	v_mfma_f32_16x16x32_bf16 v[92:95], v[154:157], v[214:217], v[92:95]
	s_waitcnt lgkmcnt(0)
	v_mfma_f32_16x16x32_bf16 v[84:87], v[146:149], v[228:231], v[84:87]
	v_mfma_f32_16x16x32_bf16 v[76:79], v[154:157], v[228:231], v[76:79]
	v_mfma_f32_16x16x32_bf16 v[112:115], v[158:161], v[182:185], v[112:115]
	v_mfma_f32_16x16x32_bf16 v[104:107], v[174:177], v[182:185], v[104:107]
	v_mfma_f32_16x16x32_bf16 v[96:99], v[158:161], v[202:205], v[96:99]
	v_mfma_f32_16x16x32_bf16 v[88:91], v[174:177], v[202:205], v[88:91]
	v_mfma_f32_16x16x32_bf16 v[80:83], v[158:161], v[210:213], v[80:83]
	v_mfma_f32_16x16x32_bf16 v[72:75], v[174:177], v[210:213], v[72:75]
	v_mfma_f32_16x16x32_bf16 v[68:71], v[158:161], v[224:227], v[68:71]
	v_mfma_f32_16x16x32_bf16 v[64:67], v[174:177], v[224:227], v[64:67]
	v_mfma_f32_16x16x32_bf16 v[112:115], v[162:165], v[198:201], v[112:115]
	v_mfma_f32_16x16x32_bf16 v[104:107], v[178:181], v[198:201], v[104:107]
	v_mfma_f32_16x16x32_bf16 v[96:99], v[162:165], v[206:209], v[96:99]
	v_mfma_f32_16x16x32_bf16 v[88:91], v[178:181], v[206:209], v[88:91]
	v_mfma_f32_16x16x32_bf16 v[80:83], v[162:165], v[214:217], v[80:83]
	v_mfma_f32_16x16x32_bf16 v[72:75], v[178:181], v[214:217], v[72:75]
	v_mfma_f32_16x16x32_bf16 v[68:71], v[162:165], v[228:231], v[68:71]
	v_mfma_f32_16x16x32_bf16 v[64:67], v[178:181], v[228:231], v[64:67]
	s_barrier
	s_mov_b32 m0, s13
	ds_read_b128 v[182:185], v141 offset:16384
	ds_read_b128 v[198:201], v141 offset:17408
	ds_read_b128 v[202:205], v141 offset:18432
	ds_read_b128 v[206:209], v141 offset:19456
	ds_read_b128 v[210:213], v141 offset:20480
	ds_read_b128 v[214:217], v141 offset:21504
	ds_read_b128 v[224:227], v141 offset:22528
	ds_read_b128 v[228:231], v141 offset:23552
	buffer_load_dwordx4 v129, s[56:59], s41 offen lds
	s_mov_b32 m0, s14
	s_add_i32 s43, s41, 0x20000
	buffer_load_dwordx4 v131, s[56:59], s41 offen lds
	s_mov_b32 m0, s15
	s_nop 0
	buffer_load_dwordx4 v129, s[56:59], s43 offen lds
	s_mov_b32 m0, s18
	s_nop 0
	buffer_load_dwordx4 v131, s[56:59], s43 offen lds
	s_mov_b32 m0, s12
	s_nop 0
	buffer_load_dwordx4 v128, s[56:59], s42 offen lds
	s_mov_b32 m0, s19
	s_nop 0
	buffer_load_dwordx4 v130, s[56:59], s42 offen lds
	s_waitcnt vmcnt(8)
	s_waitcnt lgkmcnt(0)
	s_barrier
	s_waitcnt lgkmcnt(7)
	v_mfma_f32_16x16x32_bf16 v[60:63], v[142:145], v[182:185], v[60:63]
	v_mfma_f32_16x16x32_bf16 v[56:59], v[150:153], v[182:185], v[56:59]
	s_waitcnt lgkmcnt(5)
	v_mfma_f32_16x16x32_bf16 v[52:55], v[142:145], v[202:205], v[52:55]
	v_mfma_f32_16x16x32_bf16 v[44:47], v[150:153], v[202:205], v[44:47]
	s_waitcnt lgkmcnt(3)
	v_mfma_f32_16x16x32_bf16 v[36:39], v[142:145], v[210:213], v[36:39]
	v_mfma_f32_16x16x32_bf16 v[28:31], v[150:153], v[210:213], v[28:31]
	s_waitcnt lgkmcnt(1)
	v_mfma_f32_16x16x32_bf16 v[20:23], v[142:145], v[224:227], v[20:23]
	v_mfma_f32_16x16x32_bf16 v[12:15], v[150:153], v[224:227], v[12:15]
	v_mfma_f32_16x16x32_bf16 v[60:63], v[146:149], v[198:201], v[60:63]
	v_mfma_f32_16x16x32_bf16 v[56:59], v[154:157], v[198:201], v[56:59]
	v_mfma_f32_16x16x32_bf16 v[52:55], v[146:149], v[206:209], v[52:55]
	v_mfma_f32_16x16x32_bf16 v[44:47], v[154:157], v[206:209], v[44:47]
	v_mfma_f32_16x16x32_bf16 v[36:39], v[146:149], v[214:217], v[36:39]
	v_mfma_f32_16x16x32_bf16 v[28:31], v[154:157], v[214:217], v[28:31]
	s_waitcnt lgkmcnt(0)
	v_mfma_f32_16x16x32_bf16 v[20:23], v[146:149], v[228:231], v[20:23]
	v_mfma_f32_16x16x32_bf16 v[12:15], v[154:157], v[228:231], v[12:15]
	v_mfma_f32_16x16x32_bf16 v[48:51], v[158:161], v[182:185], v[48:51]
	v_mfma_f32_16x16x32_bf16 v[40:43], v[174:177], v[182:185], v[40:43]
	v_mfma_f32_16x16x32_bf16 v[32:35], v[158:161], v[202:205], v[32:35]
	v_mfma_f32_16x16x32_bf16 v[24:27], v[174:177], v[202:205], v[24:27]
	v_mfma_f32_16x16x32_bf16 v[16:19], v[158:161], v[210:213], v[16:19]
	v_mfma_f32_16x16x32_bf16 v[8:11], v[174:177], v[210:213], v[8:11]
	v_mfma_f32_16x16x32_bf16 v[4:7], v[158:161], v[224:227], v[4:7]
	v_mfma_f32_16x16x32_bf16 v[0:3], v[174:177], v[224:227], v[0:3]
	v_mfma_f32_16x16x32_bf16 v[48:51], v[162:165], v[198:201], v[48:51]
	v_mfma_f32_16x16x32_bf16 v[40:43], v[178:181], v[198:201], v[40:43]
	v_mfma_f32_16x16x32_bf16 v[32:35], v[162:165], v[206:209], v[32:35]
	v_mfma_f32_16x16x32_bf16 v[24:27], v[178:181], v[206:209], v[24:27]
	v_mfma_f32_16x16x32_bf16 v[16:19], v[162:165], v[214:217], v[16:19]
	v_mfma_f32_16x16x32_bf16 v[8:11], v[178:181], v[214:217], v[8:11]
	v_mfma_f32_16x16x32_bf16 v[4:7], v[162:165], v[228:231], v[4:7]
	v_mfma_f32_16x16x32_bf16 v[0:3], v[178:181], v[228:231], v[0:3]
	s_barrier
	ds_read_b128 v[142:145], v140 offset:32768
	ds_read_b128 v[146:149], v140 offset:33792
	ds_read_b128 v[150:153], v140 offset:34816
	ds_read_b128 v[154:157], v140 offset:35840
	ds_read_b128 v[158:161], v140 offset:49152
	ds_read_b128 v[162:165], v140 offset:50176
	ds_read_b128 v[174:177], v140 offset:51200
	ds_read_b128 v[178:181], v140 offset:52224
	s_add_i32 s42, s42, 0x80000
	s_mov_b32 m0, s20
	ds_read_b128 v[182:185], v141 offset:32768
	ds_read_b128 v[198:201], v141 offset:33792
	ds_read_b128 v[202:205], v141 offset:34816
	ds_read_b128 v[206:209], v141 offset:35840
	ds_read_b128 v[210:213], v141 offset:36864
	ds_read_b128 v[214:217], v141 offset:37888
	ds_read_b128 v[224:227], v141 offset:38912
	ds_read_b128 v[228:231], v141 offset:39936
	buffer_load_dwordx4 v128, s[56:59], s42 offen lds
	s_mov_b32 m0, s21
	s_nop 0
	buffer_load_dwordx4 v130, s[56:59], s42 offen lds
	s_waitcnt vmcnt(8)
	s_waitcnt lgkmcnt(0)
	s_barrier
	s_waitcnt lgkmcnt(7)
	v_mfma_f32_16x16x32_bf16 v[124:127], v[142:145], v[182:185], v[124:127]
	v_mfma_f32_16x16x32_bf16 v[120:123], v[150:153], v[182:185], v[120:123]
	s_waitcnt lgkmcnt(5)
	v_mfma_f32_16x16x32_bf16 v[116:119], v[142:145], v[202:205], v[116:119]
	v_mfma_f32_16x16x32_bf16 v[108:111], v[150:153], v[202:205], v[108:111]
	s_waitcnt lgkmcnt(3)
	v_mfma_f32_16x16x32_bf16 v[100:103], v[142:145], v[210:213], v[100:103]
	v_mfma_f32_16x16x32_bf16 v[92:95], v[150:153], v[210:213], v[92:95]
	s_waitcnt lgkmcnt(1)
	v_mfma_f32_16x16x32_bf16 v[84:87], v[142:145], v[224:227], v[84:87]
	v_mfma_f32_16x16x32_bf16 v[76:79], v[150:153], v[224:227], v[76:79]
	v_mfma_f32_16x16x32_bf16 v[124:127], v[146:149], v[198:201], v[124:127]
	v_mfma_f32_16x16x32_bf16 v[120:123], v[154:157], v[198:201], v[120:123]
	v_mfma_f32_16x16x32_bf16 v[116:119], v[146:149], v[206:209], v[116:119]
	v_mfma_f32_16x16x32_bf16 v[108:111], v[154:157], v[206:209], v[108:111]
	v_mfma_f32_16x16x32_bf16 v[100:103], v[146:149], v[214:217], v[100:103]
	v_mfma_f32_16x16x32_bf16 v[92:95], v[154:157], v[214:217], v[92:95]
	s_waitcnt lgkmcnt(0)
	v_mfma_f32_16x16x32_bf16 v[84:87], v[146:149], v[228:231], v[84:87]
	v_mfma_f32_16x16x32_bf16 v[76:79], v[154:157], v[228:231], v[76:79]
	v_mfma_f32_16x16x32_bf16 v[112:115], v[158:161], v[182:185], v[112:115]
	v_mfma_f32_16x16x32_bf16 v[104:107], v[174:177], v[182:185], v[104:107]
	v_mfma_f32_16x16x32_bf16 v[96:99], v[158:161], v[202:205], v[96:99]
	v_mfma_f32_16x16x32_bf16 v[88:91], v[174:177], v[202:205], v[88:91]
	v_mfma_f32_16x16x32_bf16 v[80:83], v[158:161], v[210:213], v[80:83]
	v_mfma_f32_16x16x32_bf16 v[72:75], v[174:177], v[210:213], v[72:75]
	v_mfma_f32_16x16x32_bf16 v[68:71], v[158:161], v[224:227], v[68:71]
	v_mfma_f32_16x16x32_bf16 v[64:67], v[174:177], v[224:227], v[64:67]
	v_mfma_f32_16x16x32_bf16 v[112:115], v[162:165], v[198:201], v[112:115]
	v_mfma_f32_16x16x32_bf16 v[104:107], v[178:181], v[198:201], v[104:107]
	v_mfma_f32_16x16x32_bf16 v[96:99], v[162:165], v[206:209], v[96:99]
	v_mfma_f32_16x16x32_bf16 v[88:91], v[178:181], v[206:209], v[88:91]
	v_mfma_f32_16x16x32_bf16 v[80:83], v[162:165], v[214:217], v[80:83]
	v_mfma_f32_16x16x32_bf16 v[72:75], v[178:181], v[214:217], v[72:75]
	v_mfma_f32_16x16x32_bf16 v[68:71], v[162:165], v[228:231], v[68:71]
	v_mfma_f32_16x16x32_bf16 v[64:67], v[178:181], v[228:231], v[64:67]
	s_barrier
	s_mov_b32 m0, s22
	s_add_i32 s42, s41, 0x80
	ds_read_b128 v[182:185], v141 offset:49152
	ds_read_b128 v[198:201], v141 offset:50176
	ds_read_b128 v[202:205], v141 offset:51200
	ds_read_b128 v[206:209], v141 offset:52224
	ds_read_b128 v[210:213], v141 offset:53248
	ds_read_b128 v[214:217], v141 offset:54272
	ds_read_b128 v[224:227], v141 offset:55296
	ds_read_b128 v[228:231], v141 offset:56320
	buffer_load_dwordx4 v129, s[56:59], s42 offen lds
	s_mov_b32 m0, s23
	s_add_i32 s41, s41, 0x20080
	buffer_load_dwordx4 v131, s[56:59], s42 offen lds
	s_mov_b32 m0, s26
	s_nop 0
	buffer_load_dwordx4 v129, s[56:59], s41 offen lds
	s_mov_b32 m0, s27
	s_nop 0
	buffer_load_dwordx4 v131, s[56:59], s41 offen lds
	s_mov_b32 m0, s24
	s_nop 0
	buffer_load_dwordx4 v128, s[56:59], s40 offen lds
	s_mov_b32 m0, s25
	s_nop 0
	buffer_load_dwordx4 v130, s[56:59], s40 offen lds
	s_waitcnt vmcnt(8)
	s_waitcnt lgkmcnt(0)
	s_barrier
	s_waitcnt lgkmcnt(7)
	v_mfma_f32_16x16x32_bf16 v[60:63], v[142:145], v[182:185], v[60:63]
	v_mfma_f32_16x16x32_bf16 v[56:59], v[150:153], v[182:185], v[56:59]
	s_waitcnt lgkmcnt(5)
	v_mfma_f32_16x16x32_bf16 v[52:55], v[142:145], v[202:205], v[52:55]
	v_mfma_f32_16x16x32_bf16 v[44:47], v[150:153], v[202:205], v[44:47]
	s_waitcnt lgkmcnt(3)
	v_mfma_f32_16x16x32_bf16 v[36:39], v[142:145], v[210:213], v[36:39]
	v_mfma_f32_16x16x32_bf16 v[28:31], v[150:153], v[210:213], v[28:31]
	s_waitcnt lgkmcnt(1)
	v_mfma_f32_16x16x32_bf16 v[20:23], v[142:145], v[224:227], v[20:23]
	v_mfma_f32_16x16x32_bf16 v[12:15], v[150:153], v[224:227], v[12:15]
	v_mfma_f32_16x16x32_bf16 v[60:63], v[146:149], v[198:201], v[60:63]
	v_mfma_f32_16x16x32_bf16 v[56:59], v[154:157], v[198:201], v[56:59]
	v_mfma_f32_16x16x32_bf16 v[52:55], v[146:149], v[206:209], v[52:55]
	v_mfma_f32_16x16x32_bf16 v[44:47], v[154:157], v[206:209], v[44:47]
	v_mfma_f32_16x16x32_bf16 v[36:39], v[146:149], v[214:217], v[36:39]
	v_mfma_f32_16x16x32_bf16 v[28:31], v[154:157], v[214:217], v[28:31]
	s_waitcnt lgkmcnt(0)
	v_mfma_f32_16x16x32_bf16 v[20:23], v[146:149], v[228:231], v[20:23]
	v_mfma_f32_16x16x32_bf16 v[12:15], v[154:157], v[228:231], v[12:15]
	v_mfma_f32_16x16x32_bf16 v[48:51], v[158:161], v[182:185], v[48:51]
	v_mfma_f32_16x16x32_bf16 v[40:43], v[174:177], v[182:185], v[40:43]
	v_mfma_f32_16x16x32_bf16 v[32:35], v[158:161], v[202:205], v[32:35]
	v_mfma_f32_16x16x32_bf16 v[24:27], v[174:177], v[202:205], v[24:27]
	v_mfma_f32_16x16x32_bf16 v[16:19], v[158:161], v[210:213], v[16:19]
	v_mfma_f32_16x16x32_bf16 v[8:11], v[174:177], v[210:213], v[8:11]
	v_mfma_f32_16x16x32_bf16 v[4:7], v[158:161], v[224:227], v[4:7]
	v_mfma_f32_16x16x32_bf16 v[0:3], v[174:177], v[224:227], v[0:3]
	v_mfma_f32_16x16x32_bf16 v[48:51], v[162:165], v[198:201], v[48:51]
	v_mfma_f32_16x16x32_bf16 v[40:43], v[178:181], v[198:201], v[40:43]
	v_mfma_f32_16x16x32_bf16 v[32:35], v[162:165], v[206:209], v[32:35]
	v_mfma_f32_16x16x32_bf16 v[24:27], v[178:181], v[206:209], v[24:27]
	v_mfma_f32_16x16x32_bf16 v[16:19], v[162:165], v[214:217], v[16:19]
	v_mfma_f32_16x16x32_bf16 v[8:11], v[178:181], v[214:217], v[8:11]
	v_mfma_f32_16x16x32_bf16 v[4:7], v[162:165], v[228:231], v[4:7]
	v_mfma_f32_16x16x32_bf16 v[0:3], v[178:181], v[228:231], v[0:3]
	s_barrier
	s_add_i32 s37, s37, 2
	s_addk_i32 s10, 0x100
	s_addk_i32 s11, 0x100
	s_cmp_gt_u32 s37, 5
	s_cbranch_scc0 .LBB0_1238
	s_and_b64 vcc, exec, s[2:3]
	s_cbranch_vccz .LBB0_1241
	s_barrier

.LBB0_1443:
	ds_read_b128 v[16:19], v186
	ds_read_b128 v[20:23], v186 offset:1024
	ds_read_b128 v[24:27], v186 offset:2048
	ds_read_b128 v[28:31], v186 offset:3072
	ds_read_b128 v[0:3], v186 offset:16384
	ds_read_b128 v[4:7], v186 offset:17408
	ds_read_b128 v[8:11], v186 offset:18432
	ds_read_b128 v[12:15], v186 offset:19456
	s_add_i32 s72, s0, 0xfffc0080
	s_cmp_eq_u32 s81, 12
	s_cselect_b32 vcc_lo, s96, s72
	s_cselect_b32 s83, s97, s1
	s_add_i32 s82, vcc_lo, 0x80
	s_mov_b32 s56, s26
	s_mov_b32 m0, s87
	ds_read_b128 v[174:177], v198
	ds_read_b128 v[178:181], v198 offset:1024
	ds_read_b128 v[200:203], v198 offset:2048
	ds_read_b128 v[204:207], v198 offset:3072
	ds_read_b128 v[208:211], v198 offset:4096
	ds_read_b128 v[212:215], v198 offset:5120
	ds_read_b128 v[224:227], v198 offset:6144
	ds_read_b128 v[228:231], v198 offset:7168
	buffer_load_dwordx4 v160, s[56:59], s0 offen lds
	s_mov_b32 m0, s88
	s_nop 0
	buffer_load_dwordx4 v162, s[56:59], s0 offen lds
	s_waitcnt vmcnt(8)
	s_waitcnt lgkmcnt(0)
	s_barrier
	s_waitcnt lgkmcnt(6)
	v_mfma_f32_16x16x128_f8f6f4 v[156:159], v[16:23], v[174:181], v[156:159]
	v_mfma_f32_16x16x128_f8f6f4 v[148:151], v[24:31], v[174:181], v[148:151]
	s_waitcnt lgkmcnt(4)
	v_mfma_f32_16x16x128_f8f6f4 v[140:143], v[16:23], v[200:207], v[140:143]
	v_mfma_f32_16x16x128_f8f6f4 v[132:135], v[24:31], v[200:207], v[132:135]
	s_waitcnt lgkmcnt(2)
	v_mfma_f32_16x16x128_f8f6f4 v[124:127], v[16:23], v[208:215], v[124:127]
	v_mfma_f32_16x16x128_f8f6f4 v[116:119], v[24:31], v[208:215], v[116:119]
	s_waitcnt lgkmcnt(0)
	v_mfma_f32_16x16x128_f8f6f4 v[108:111], v[16:23], v[224:231], v[108:111]
	v_mfma_f32_16x16x128_f8f6f4 v[100:103], v[24:31], v[224:231], v[100:103]
	v_mfma_f32_16x16x128_f8f6f4 v[152:155], v[0:7], v[174:181], v[152:155]
	v_mfma_f32_16x16x128_f8f6f4 v[144:147], v[8:15], v[174:181], v[144:147]
	v_mfma_f32_16x16x128_f8f6f4 v[136:139], v[0:7], v[200:207], v[136:139]
	v_mfma_f32_16x16x128_f8f6f4 v[128:131], v[8:15], v[200:207], v[128:131]
	v_mfma_f32_16x16x128_f8f6f4 v[120:123], v[0:7], v[208:215], v[120:123]
	v_mfma_f32_16x16x128_f8f6f4 v[112:115], v[8:15], v[208:215], v[112:115]
	v_mfma_f32_16x16x128_f8f6f4 v[104:107], v[0:7], v[224:231], v[104:107]
	v_mfma_f32_16x16x128_f8f6f4 v[96:99], v[8:15], v[224:231], v[96:99]
	s_barrier
	s_mov_b32 m0, s46
	ds_read_b128 v[174:177], v198 offset:16384
	ds_read_b128 v[178:181], v198 offset:17408
	ds_read_b128 v[200:203], v198 offset:18432
	ds_read_b128 v[204:207], v198 offset:19456
	ds_read_b128 v[208:211], v198 offset:20480
	ds_read_b128 v[212:215], v198 offset:21504
	ds_read_b128 v[224:227], v198 offset:22528
	ds_read_b128 v[228:231], v198 offset:23552
	buffer_load_dwordx4 v161, s[56:59], s83 offen lds
	s_mov_b32 m0, s47
	s_add_i32 vcc_hi, s83, 0x40000
	buffer_load_dwordx4 v163, s[56:59], s83 offen lds
	s_mov_b32 m0, s48
	s_nop 0
	buffer_load_dwordx4 v161, s[56:59], vcc_hi offen lds
	s_mov_b32 m0, s49
	s_nop 0
	buffer_load_dwordx4 v163, s[56:59], vcc_hi offen lds
	s_mov_b32 m0, s45
	s_nop 0
	buffer_load_dwordx4 v160, s[56:59], vcc_lo offen lds
	s_mov_b32 m0, s50
	s_nop 0
	buffer_load_dwordx4 v162, s[56:59], vcc_lo offen lds
	s_waitcnt vmcnt(8)
	s_waitcnt lgkmcnt(0)
	s_barrier
	s_waitcnt lgkmcnt(6)
	v_mfma_f32_16x16x128_f8f6f4 v[92:95], v[16:23], v[174:181], v[92:95]
	v_mfma_f32_16x16x128_f8f6f4 v[84:87], v[24:31], v[174:181], v[84:87]
	s_waitcnt lgkmcnt(4)
	v_mfma_f32_16x16x128_f8f6f4 v[76:79], v[16:23], v[200:207], v[76:79]
	v_mfma_f32_16x16x128_f8f6f4 v[68:71], v[24:31], v[200:207], v[68:71]
	s_waitcnt lgkmcnt(2)
	v_mfma_f32_16x16x128_f8f6f4 v[60:63], v[16:23], v[208:215], v[60:63]
	v_mfma_f32_16x16x128_f8f6f4 v[52:55], v[24:31], v[208:215], v[52:55]
	s_waitcnt lgkmcnt(0)
	v_mfma_f32_16x16x128_f8f6f4 v[44:47], v[16:23], v[224:231], v[44:47]
	v_mfma_f32_16x16x128_f8f6f4 v[36:39], v[24:31], v[224:231], v[36:39]
	v_mfma_f32_16x16x128_f8f6f4 v[88:91], v[0:7], v[174:181], v[88:91]
	v_mfma_f32_16x16x128_f8f6f4 v[80:83], v[8:15], v[174:181], v[80:83]
	v_mfma_f32_16x16x128_f8f6f4 v[72:75], v[0:7], v[200:207], v[72:75]
	v_mfma_f32_16x16x128_f8f6f4 v[64:67], v[8:15], v[200:207], v[64:67]
	v_mfma_f32_16x16x128_f8f6f4 v[56:59], v[0:7], v[208:215], v[56:59]
	v_mfma_f32_16x16x128_f8f6f4 v[48:51], v[8:15], v[208:215], v[48:51]
	v_mfma_f32_16x16x128_f8f6f4 v[40:43], v[0:7], v[224:231], v[40:43]
	v_mfma_f32_16x16x128_f8f6f4 v[32:35], v[8:15], v[224:231], v[32:35]
	s_barrier
	ds_read_b128 v[0:3], v186 offset:32768
	ds_read_b128 v[4:7], v186 offset:33792
	ds_read_b128 v[8:11], v186 offset:34816
	ds_read_b128 v[12:15], v186 offset:35840
	ds_read_b128 v[16:19], v186 offset:49152
	ds_read_b128 v[20:23], v186 offset:50176
	ds_read_b128 v[24:27], v186 offset:51200
	ds_read_b128 v[28:31], v186 offset:52224
	s_add_i32 vcc_lo, vcc_lo, 0x40000
	s_mov_b32 m0, s51
	ds_read_b128 v[174:177], v198 offset:32768
	ds_read_b128 v[178:181], v198 offset:33792
	ds_read_b128 v[200:203], v198 offset:34816
	ds_read_b128 v[204:207], v198 offset:35840
	ds_read_b128 v[208:211], v198 offset:36864
	ds_read_b128 v[212:215], v198 offset:37888
	ds_read_b128 v[224:227], v198 offset:38912
	ds_read_b128 v[228:231], v198 offset:39936
	buffer_load_dwordx4 v160, s[56:59], vcc_lo offen lds
	s_mov_b32 m0, s52
	s_nop 0
	buffer_load_dwordx4 v162, s[56:59], vcc_lo offen lds
	s_waitcnt vmcnt(8)
	s_waitcnt lgkmcnt(0)
	s_barrier
	s_waitcnt lgkmcnt(6)
	v_mfma_f32_16x16x128_f8f6f4 v[156:159], v[0:7], v[174:181], v[156:159]
	v_mfma_f32_16x16x128_f8f6f4 v[148:151], v[8:15], v[174:181], v[148:151]
	s_waitcnt lgkmcnt(4)
	v_mfma_f32_16x16x128_f8f6f4 v[140:143], v[0:7], v[200:207], v[140:143]
	v_mfma_f32_16x16x128_f8f6f4 v[132:135], v[8:15], v[200:207], v[132:135]
	s_waitcnt lgkmcnt(2)
	v_mfma_f32_16x16x128_f8f6f4 v[124:127], v[0:7], v[208:215], v[124:127]
	v_mfma_f32_16x16x128_f8f6f4 v[116:119], v[8:15], v[208:215], v[116:119]
	s_waitcnt lgkmcnt(0)
	v_mfma_f32_16x16x128_f8f6f4 v[108:111], v[0:7], v[224:231], v[108:111]
	v_mfma_f32_16x16x128_f8f6f4 v[100:103], v[8:15], v[224:231], v[100:103]
	v_mfma_f32_16x16x128_f8f6f4 v[152:155], v[16:23], v[174:181], v[152:155]
	v_mfma_f32_16x16x128_f8f6f4 v[144:147], v[24:31], v[174:181], v[144:147]
	v_mfma_f32_16x16x128_f8f6f4 v[136:139], v[16:23], v[200:207], v[136:139]
	v_mfma_f32_16x16x128_f8f6f4 v[128:131], v[24:31], v[200:207], v[128:131]
	v_mfma_f32_16x16x128_f8f6f4 v[120:123], v[16:23], v[208:215], v[120:123]
	v_mfma_f32_16x16x128_f8f6f4 v[112:115], v[24:31], v[208:215], v[112:115]
	v_mfma_f32_16x16x128_f8f6f4 v[104:107], v[16:23], v[224:231], v[104:107]
	v_mfma_f32_16x16x128_f8f6f4 v[96:99], v[24:31], v[224:231], v[96:99]
	s_barrier
	s_mov_b32 m0, s76
	s_add_i32 vcc_lo, s83, 0x80
	ds_read_b128 v[174:177], v198 offset:49152
	ds_read_b128 v[178:181], v198 offset:50176
	ds_read_b128 v[200:203], v198 offset:51200
	ds_read_b128 v[204:207], v198 offset:52224
	ds_read_b128 v[208:211], v198 offset:53248
	ds_read_b128 v[212:215], v198 offset:54272
	ds_read_b128 v[224:227], v198 offset:55296
	ds_read_b128 v[228:231], v198 offset:56320
	buffer_load_dwordx4 v161, s[56:59], vcc_lo offen lds
	s_mov_b32 m0, s77
	s_add_i32 s83, s83, 0x40080
	buffer_load_dwordx4 v163, s[56:59], vcc_lo offen lds
	s_mov_b32 m0, s85
	s_nop 0
	buffer_load_dwordx4 v161, s[56:59], s83 offen lds
	s_mov_b32 m0, s86
	s_nop 0
	buffer_load_dwordx4 v163, s[56:59], s83 offen lds
	s_mov_b32 m0, s78
	s_nop 0
	buffer_load_dwordx4 v160, s[56:59], s82 offen lds
	s_mov_b32 m0, s79
	s_nop 0
	buffer_load_dwordx4 v162, s[56:59], s82 offen lds
	s_waitcnt vmcnt(8)
	s_waitcnt lgkmcnt(0)
	s_barrier
	s_waitcnt lgkmcnt(6)
	v_mfma_f32_16x16x128_f8f6f4 v[92:95], v[0:7], v[174:181], v[92:95]
	v_mfma_f32_16x16x128_f8f6f4 v[84:87], v[8:15], v[174:181], v[84:87]
	s_waitcnt lgkmcnt(4)
	v_mfma_f32_16x16x128_f8f6f4 v[76:79], v[0:7], v[200:207], v[76:79]
	v_mfma_f32_16x16x128_f8f6f4 v[68:71], v[8:15], v[200:207], v[68:71]
	s_waitcnt lgkmcnt(2)
	v_mfma_f32_16x16x128_f8f6f4 v[60:63], v[0:7], v[208:215], v[60:63]
	v_mfma_f32_16x16x128_f8f6f4 v[52:55], v[8:15], v[208:215], v[52:55]
	s_waitcnt lgkmcnt(0)
	v_mfma_f32_16x16x128_f8f6f4 v[44:47], v[0:7], v[224:231], v[44:47]
	v_mfma_f32_16x16x128_f8f6f4 v[36:39], v[8:15], v[224:231], v[36:39]
	v_mfma_f32_16x16x128_f8f6f4 v[88:91], v[16:23], v[174:181], v[88:91]
	v_mfma_f32_16x16x128_f8f6f4 v[80:83], v[24:31], v[174:181], v[80:83]
	v_mfma_f32_16x16x128_f8f6f4 v[72:75], v[16:23], v[200:207], v[72:75]
	v_mfma_f32_16x16x128_f8f6f4 v[64:67], v[24:31], v[200:207], v[64:67]
	v_mfma_f32_16x16x128_f8f6f4 v[56:59], v[16:23], v[208:215], v[56:59]
	v_mfma_f32_16x16x128_f8f6f4 v[48:51], v[24:31], v[208:215], v[48:51]
	v_mfma_f32_16x16x128_f8f6f4 v[40:43], v[16:23], v[224:231], v[40:43]
	v_mfma_f32_16x16x128_f8f6f4 v[32:35], v[24:31], v[224:231], v[32:35]
	s_barrier
	s_add_i32 s81, s81, 2
	s_addk_i32 s0, 0x100
	s_addk_i32 s1, 0x100
	s_cmp_gt_u32 s81, 13
	s_cbranch_scc0 .LBB0_1443
	s_and_b64 vcc, exec, s[70:71]
	s_cbranch_vccz .LBB0_1446
	s_barrier

.LBB0_1667:
	ds_read_b128 v[16:19], v198
	ds_read_b128 v[20:23], v198 offset:1024
	ds_read_b128 v[24:27], v198 offset:2048
	ds_read_b128 v[28:31], v198 offset:3072
	ds_read_b128 v[0:3], v198 offset:16384
	ds_read_b128 v[4:7], v198 offset:17408
	ds_read_b128 v[8:11], v198 offset:18432
	ds_read_b128 v[12:15], v198 offset:19456
	s_add_i32 s55, s0, 0xfffd0080
	s_cmp_eq_u32 s33, 8
	s_cselect_b32 s81, s40, s55
	s_cselect_b32 s80, s41, s1
	s_add_i32 s55, s81, 0x80
	s_mov_b32 s56, s78
	s_mov_b32 m0, s20
	ds_read_b128 v[174:177], v199
	ds_read_b128 v[178:181], v199 offset:1024
	ds_read_b128 v[200:203], v199 offset:2048
	ds_read_b128 v[204:207], v199 offset:3072
	ds_read_b128 v[208:211], v199 offset:4096
	ds_read_b128 v[212:215], v199 offset:5120
	ds_read_b128 v[224:227], v199 offset:6144
	ds_read_b128 v[228:231], v199 offset:7168
	buffer_load_dwordx4 v162, s[56:59], s0 offen lds
	s_mov_b32 m0, s19
	s_nop 0
	buffer_load_dwordx4 v164, s[56:59], s0 offen lds
	s_waitcnt vmcnt(8)
	s_waitcnt lgkmcnt(0)
	s_barrier
	s_waitcnt lgkmcnt(6)
	v_mfma_f32_16x16x128_f8f6f4 v[156:159], v[16:23], v[174:181], v[156:159]
	v_mfma_f32_16x16x128_f8f6f4 v[152:155], v[24:31], v[174:181], v[152:155]
	s_waitcnt lgkmcnt(4)
	v_mfma_f32_16x16x128_f8f6f4 v[140:143], v[16:23], v[200:207], v[140:143]
	v_mfma_f32_16x16x128_f8f6f4 v[136:139], v[24:31], v[200:207], v[136:139]
	s_waitcnt lgkmcnt(2)
	v_mfma_f32_16x16x128_f8f6f4 v[124:127], v[16:23], v[208:215], v[124:127]
	v_mfma_f32_16x16x128_f8f6f4 v[120:123], v[24:31], v[208:215], v[120:123]
	s_waitcnt lgkmcnt(0)
	v_mfma_f32_16x16x128_f8f6f4 v[108:111], v[16:23], v[224:231], v[108:111]
	v_mfma_f32_16x16x128_f8f6f4 v[104:107], v[24:31], v[224:231], v[104:107]
	v_mfma_f32_16x16x128_f8f6f4 v[148:151], v[0:7], v[174:181], v[148:151]
	v_mfma_f32_16x16x128_f8f6f4 v[144:147], v[8:15], v[174:181], v[144:147]
	v_mfma_f32_16x16x128_f8f6f4 v[132:135], v[0:7], v[200:207], v[132:135]
	v_mfma_f32_16x16x128_f8f6f4 v[128:131], v[8:15], v[200:207], v[128:131]
	v_mfma_f32_16x16x128_f8f6f4 v[116:119], v[0:7], v[208:215], v[116:119]
	v_mfma_f32_16x16x128_f8f6f4 v[112:115], v[8:15], v[208:215], v[112:115]
	v_mfma_f32_16x16x128_f8f6f4 v[100:103], v[0:7], v[224:231], v[100:103]
	v_mfma_f32_16x16x128_f8f6f4 v[96:99], v[8:15], v[224:231], v[96:99]
	s_barrier
	s_mov_b32 m0, s85
	ds_read_b128 v[174:177], v199 offset:16384
	ds_read_b128 v[178:181], v199 offset:17408
	ds_read_b128 v[200:203], v199 offset:18432
	ds_read_b128 v[204:207], v199 offset:19456
	ds_read_b128 v[208:211], v199 offset:20480
	ds_read_b128 v[212:215], v199 offset:21504
	ds_read_b128 v[224:227], v199 offset:22528
	ds_read_b128 v[228:231], v199 offset:23552
	buffer_load_dwordx4 v161, s[56:59], s80 offen lds
	s_mov_b32 m0, s86
	s_add_i32 s82, s80, 0x30000
	buffer_load_dwordx4 v163, s[56:59], s80 offen lds
	s_mov_b32 m0, s87
	s_nop 0
	buffer_load_dwordx4 v161, s[56:59], s82 offen lds
	s_mov_b32 m0, s88
	s_nop 0
	buffer_load_dwordx4 v163, s[56:59], s82 offen lds
	s_mov_b32 m0, s18
	s_nop 0
	buffer_load_dwordx4 v162, s[56:59], s81 offen lds
	s_mov_b32 m0, s89
	s_nop 0
	buffer_load_dwordx4 v164, s[56:59], s81 offen lds
	s_waitcnt vmcnt(8)
	s_waitcnt lgkmcnt(0)
	s_barrier
	s_waitcnt lgkmcnt(6)
	v_mfma_f32_16x16x128_f8f6f4 v[92:95], v[16:23], v[174:181], v[92:95]
	v_mfma_f32_16x16x128_f8f6f4 v[88:91], v[24:31], v[174:181], v[88:91]
	s_waitcnt lgkmcnt(4)
	v_mfma_f32_16x16x128_f8f6f4 v[76:79], v[16:23], v[200:207], v[76:79]
	v_mfma_f32_16x16x128_f8f6f4 v[72:75], v[24:31], v[200:207], v[72:75]
	s_waitcnt lgkmcnt(2)
	v_mfma_f32_16x16x128_f8f6f4 v[60:63], v[16:23], v[208:215], v[60:63]
	v_mfma_f32_16x16x128_f8f6f4 v[56:59], v[24:31], v[208:215], v[56:59]
	s_waitcnt lgkmcnt(0)
	v_mfma_f32_16x16x128_f8f6f4 v[44:47], v[16:23], v[224:231], v[44:47]
	v_mfma_f32_16x16x128_f8f6f4 v[40:43], v[24:31], v[224:231], v[40:43]
	v_mfma_f32_16x16x128_f8f6f4 v[84:87], v[0:7], v[174:181], v[84:87]
	v_mfma_f32_16x16x128_f8f6f4 v[80:83], v[8:15], v[174:181], v[80:83]
	v_mfma_f32_16x16x128_f8f6f4 v[68:71], v[0:7], v[200:207], v[68:71]
	v_mfma_f32_16x16x128_f8f6f4 v[64:67], v[8:15], v[200:207], v[64:67]
	v_mfma_f32_16x16x128_f8f6f4 v[52:55], v[0:7], v[208:215], v[52:55]
	v_mfma_f32_16x16x128_f8f6f4 v[48:51], v[8:15], v[208:215], v[48:51]
	v_mfma_f32_16x16x128_f8f6f4 v[36:39], v[0:7], v[224:231], v[36:39]
	v_mfma_f32_16x16x128_f8f6f4 v[32:35], v[8:15], v[224:231], v[32:35]
	s_barrier
	ds_read_b128 v[0:3], v198 offset:32768
	ds_read_b128 v[4:7], v198 offset:33792
	ds_read_b128 v[8:11], v198 offset:34816
	ds_read_b128 v[12:15], v198 offset:35840
	ds_read_b128 v[16:19], v198 offset:49152
	ds_read_b128 v[20:23], v198 offset:50176
	ds_read_b128 v[24:27], v198 offset:51200
	ds_read_b128 v[28:31], v198 offset:52224
	s_add_i32 s81, s81, 0x30000
	s_mov_b32 m0, s91
	ds_read_b128 v[174:177], v199 offset:32768
	ds_read_b128 v[178:181], v199 offset:33792
	ds_read_b128 v[200:203], v199 offset:34816
	ds_read_b128 v[204:207], v199 offset:35840
	ds_read_b128 v[208:211], v199 offset:36864
	ds_read_b128 v[212:215], v199 offset:37888
	ds_read_b128 v[224:227], v199 offset:38912
	ds_read_b128 v[228:231], v199 offset:39936
	buffer_load_dwordx4 v162, s[56:59], s81 offen lds
	s_mov_b32 m0, s92
	s_nop 0
	buffer_load_dwordx4 v164, s[56:59], s81 offen lds
	s_waitcnt vmcnt(8)
	s_waitcnt lgkmcnt(0)
	s_barrier
	s_waitcnt lgkmcnt(6)
	v_mfma_f32_16x16x128_f8f6f4 v[156:159], v[0:7], v[174:181], v[156:159]
	v_mfma_f32_16x16x128_f8f6f4 v[152:155], v[8:15], v[174:181], v[152:155]
	s_waitcnt lgkmcnt(4)
	v_mfma_f32_16x16x128_f8f6f4 v[140:143], v[0:7], v[200:207], v[140:143]
	v_mfma_f32_16x16x128_f8f6f4 v[136:139], v[8:15], v[200:207], v[136:139]
	s_waitcnt lgkmcnt(2)
	v_mfma_f32_16x16x128_f8f6f4 v[124:127], v[0:7], v[208:215], v[124:127]
	v_mfma_f32_16x16x128_f8f6f4 v[120:123], v[8:15], v[208:215], v[120:123]
	s_waitcnt lgkmcnt(0)
	v_mfma_f32_16x16x128_f8f6f4 v[108:111], v[0:7], v[224:231], v[108:111]
	v_mfma_f32_16x16x128_f8f6f4 v[104:107], v[8:15], v[224:231], v[104:107]
	v_mfma_f32_16x16x128_f8f6f4 v[148:151], v[16:23], v[174:181], v[148:151]
	v_mfma_f32_16x16x128_f8f6f4 v[144:147], v[24:31], v[174:181], v[144:147]
	v_mfma_f32_16x16x128_f8f6f4 v[132:135], v[16:23], v[200:207], v[132:135]
	v_mfma_f32_16x16x128_f8f6f4 v[128:131], v[24:31], v[200:207], v[128:131]
	v_mfma_f32_16x16x128_f8f6f4 v[116:119], v[16:23], v[208:215], v[116:119]
	v_mfma_f32_16x16x128_f8f6f4 v[112:115], v[24:31], v[208:215], v[112:115]
	v_mfma_f32_16x16x128_f8f6f4 v[100:103], v[16:23], v[224:231], v[100:103]
	v_mfma_f32_16x16x128_f8f6f4 v[96:99], v[24:31], v[224:231], v[96:99]
	s_barrier
	s_mov_b32 m0, s93
	s_add_i32 s81, s80, 0x80
	ds_read_b128 v[174:177], v199 offset:49152
	ds_read_b128 v[178:181], v199 offset:50176
	ds_read_b128 v[200:203], v199 offset:51200
	ds_read_b128 v[204:207], v199 offset:52224
	ds_read_b128 v[208:211], v199 offset:53248
	ds_read_b128 v[212:215], v199 offset:54272
	ds_read_b128 v[224:227], v199 offset:55296
	ds_read_b128 v[228:231], v199 offset:56320
	buffer_load_dwordx4 v161, s[56:59], s81 offen lds
	s_mov_b32 m0, s95
	s_add_i32 s80, s80, 0x30080
	buffer_load_dwordx4 v163, s[56:59], s81 offen lds
	s_mov_b32 m0, s83
	s_nop 0
	buffer_load_dwordx4 v161, s[56:59], s80 offen lds
	s_mov_b32 m0, s21
	s_nop 0
	buffer_load_dwordx4 v163, s[56:59], s80 offen lds
	s_mov_b32 m0, s96
	s_nop 0
	buffer_load_dwordx4 v162, s[56:59], s55 offen lds
	s_mov_b32 m0, s97
	s_nop 0
	buffer_load_dwordx4 v164, s[56:59], s55 offen lds
	s_waitcnt vmcnt(8)
	s_waitcnt lgkmcnt(0)
	s_barrier
	s_waitcnt lgkmcnt(6)
	v_mfma_f32_16x16x128_f8f6f4 v[92:95], v[0:7], v[174:181], v[92:95]
	v_mfma_f32_16x16x128_f8f6f4 v[88:91], v[8:15], v[174:181], v[88:91]
	s_waitcnt lgkmcnt(4)
	v_mfma_f32_16x16x128_f8f6f4 v[76:79], v[0:7], v[200:207], v[76:79]
	v_mfma_f32_16x16x128_f8f6f4 v[72:75], v[8:15], v[200:207], v[72:75]
	s_waitcnt lgkmcnt(2)
	v_mfma_f32_16x16x128_f8f6f4 v[60:63], v[0:7], v[208:215], v[60:63]
	v_mfma_f32_16x16x128_f8f6f4 v[56:59], v[8:15], v[208:215], v[56:59]
	s_waitcnt lgkmcnt(0)
	v_mfma_f32_16x16x128_f8f6f4 v[44:47], v[0:7], v[224:231], v[44:47]
	v_mfma_f32_16x16x128_f8f6f4 v[40:43], v[8:15], v[224:231], v[40:43]
	v_mfma_f32_16x16x128_f8f6f4 v[84:87], v[16:23], v[174:181], v[84:87]
	v_mfma_f32_16x16x128_f8f6f4 v[80:83], v[24:31], v[174:181], v[80:83]
	v_mfma_f32_16x16x128_f8f6f4 v[68:71], v[16:23], v[200:207], v[68:71]
	v_mfma_f32_16x16x128_f8f6f4 v[64:67], v[24:31], v[200:207], v[64:67]
	v_mfma_f32_16x16x128_f8f6f4 v[52:55], v[16:23], v[208:215], v[52:55]
	v_mfma_f32_16x16x128_f8f6f4 v[48:51], v[24:31], v[208:215], v[48:51]
	v_mfma_f32_16x16x128_f8f6f4 v[36:39], v[16:23], v[224:231], v[36:39]
	v_mfma_f32_16x16x128_f8f6f4 v[32:35], v[24:31], v[224:231], v[32:35]
	s_barrier
	s_add_i32 s33, s33, 2
	s_addk_i32 s0, 0x100
	s_addk_i32 s1, 0x100
	s_cmp_gt_u32 s33, 9
	s_cbranch_scc0 .LBB0_1667
	v_readlane_b32 s64, v253, 40
	s_and_b64 vcc, exec, s[24:25]
	v_readlane_b32 s65, v253, 41
	s_cbranch_vccz .LBB0_1670
	s_barrier
